# LoRA epilogue: one dispatch on the output kind per unit instead of scalar branches around every element (kinds 0/1 share a straight-line path with the multiplier in an SGPR; same arithmetic incl. IEEE
# baseline (speedup 1.0000x reference)
; __device__ __forceinline__ unsigned cvt_pk_bf16(float lo, float hi) { const f32x2c v = {lo, hi}; const bf16x2c b = __builtin_convertvector(v, bf16x2c); return __builtin_bit_cast(unsigned, b); }
; __device__ __forceinline__ float sigmoidf_(float x) { return 1.f / (1.f + __expf(-x)); }
;     __device__ __forceinline__ void operator()(const f32x4 (&acc)[2][2][4][2], const Unit& u, int wr, int wc, int fr, int fq) const {
;         const int row0 = u.pm * BM + wr * 64 + fr, col0 = u.pn * BM + wc * 32 + 8 * fq;
;         const int kind = u.pn >> 1;
;         bf16* O = LW + (size_t)kind * ostride;
; #pragma unroll
;         for (int bj = 0; bj < 2; ++bj) { const int col = (col0 + bj * HALF) & 511;
;             f32x4 b0 = (f32x4){0.f, 0.f, 0.f, 0.f}, b1 = b0;
;             if (kind == 0) { b0 = *(const f32x4*)(w0 + col); b1 = *(const f32x4*)(w0 + col + 4); }
;             else if (kind == 1) { b0 = *(const f32x4*)(a0 + col); b1 = *(const f32x4*)(a0 + col + 4); }
; #pragma unroll
;             for (int ai = 0; ai < 2; ++ai)
; #pragma unroll
;                 for (int m = 0; m < 4; ++m) { const size_t row = (size_t)(row0 + ai * HALF + m * 16);
;                     const f32x4 v0 = acc[ai][bj][m][0] + b0, v1 = acc[ai][bj][m][1] + b1; float o[8];
; #pragma unroll
;                     for (int e = 0; e < 8; ++e) { float x = (e < 4) ? v0[e & 3] : v1[e & 3];
;                         if (kind == 0) x = -0.6065306597126334f * sigmoidf_(x);
;                         else if (kind == 1) x = sigmoidf_(x);
;                         o[e] = x; }
;                     u32x4 w; w.x = cvt_pk_bf16(o[0], o[1]); w.y = cvt_pk_bf16(o[2], o[3]); w.z = cvt_pk_bf16(o[4], o[5]); w.w = cvt_pk_bf16(o[6], o[7]);
;                     *(u32x4*)(O + row * 512 + col) = w; } }
.LBB0_571:
	s_lshl_b32 s0, s33, 8
	s_ashr_i32 s76, s33, 1
	s_and_b32 s0, s0, 0x100
	v_or_b32_e32 v136, s0, v154
	s_ashr_i32 s77, s76, 31
	s_lshl_b64 s[2:3], s[76:77], 26
	s_add_u32 s2, s28, s2
	s_addc_u32 s3, s29, s3
	v_lshl_add_u32 v156, s68, 8, v152
	v_ashrrev_i32_e32 v157, 31, v156
	v_lshlrev_b64 v[156:157], 10, v[156:157]
	v_lshlrev_b32_e32 v158, 1, v136
	v_mov_b32_e32 v159, v137
	v_lshl_add_u64 v[156:157], v[156:157], 0, v[158:159]
	v_lshl_add_u64 v[156:157], s[2:3], 0, v[156:157]
	s_cmp_gt_u32 s33, 3
	s_cbranch_scc1 .Llora_g
	s_cmp_lt_u32 s33, 2
	s_cselect_b32 s5, s67, s71
	s_cselect_b32 s4, s66, s70
	v_lshlrev_b32_e32 v160, 2, v136
	s_nop 0
	global_load_dwordx4 v[164:167], v160, s[4:5]
	global_load_dwordx4 v[168:171], v160, s[4:5] offset:16
	global_load_dwordx4 v[172:175], v160, s[4:5] offset:512
	global_load_dwordx4 v[176:179], v160, s[4:5] offset:528
	s_cmp_lt_u32 s33, 2
	s_cselect_b32 s0, 0xbf1b4598, 1.0
	s_waitcnt vmcnt(0)
	v_pk_add_f32 v[132:133], v[132:133], v[164:165]
	v_pk_add_f32 v[134:135], v[134:135], v[166:167]
	v_pk_add_f32 v[128:129], v[128:129], v[168:169]
	v_pk_add_f32 v[130:131], v[130:131], v[170:171]
	v_mul_f32_e32 v132, 0xbfb8aa3b, v132
	v_mul_f32_e32 v133, 0xbfb8aa3b, v133
	v_mul_f32_e32 v134, 0xbfb8aa3b, v134
	v_mul_f32_e32 v135, 0xbfb8aa3b, v135
	v_mul_f32_e32 v128, 0xbfb8aa3b, v128
	v_mul_f32_e32 v129, 0xbfb8aa3b, v129
	v_mul_f32_e32 v130, 0xbfb8aa3b, v130
	v_mul_f32_e32 v131, 0xbfb8aa3b, v131
	v_exp_f32_e32 v132, v132
	v_exp_f32_e32 v133, v133
	v_exp_f32_e32 v134, v134
	v_exp_f32_e32 v135, v135
	v_exp_f32_e32 v128, v128
	v_exp_f32_e32 v129, v129
	v_exp_f32_e32 v130, v130
	v_exp_f32_e32 v131, v131
	v_pk_add_f32 v[132:133], v[132:133], 1.0 op_sel_hi:[1,0]
	v_pk_add_f32 v[134:135], v[134:135], 1.0 op_sel_hi:[1,0]
	v_pk_add_f32 v[128:129], v[128:129], 1.0 op_sel_hi:[1,0]
	v_pk_add_f32 v[130:131], v[130:131], 1.0 op_sel_hi:[1,0]
	v_div_scale_f32 v180, s[100:101], v132, v132, 1.0
	v_rcp_f32_e32 v181, v180
	v_div_scale_f32 v182, vcc, 1.0, v132, 1.0
	v_fma_f32 v183, -v180, v181, 1.0
	v_fmac_f32_e32 v181, v183, v181
	v_mul_f32_e32 v183, v182, v181
	v_fma_f32 v184, -v180, v183, v182
	v_fmac_f32_e32 v183, v184, v181
	v_fma_f32 v180, -v180, v183, v182
	v_div_fmas_f32 v180, v180, v181, v183
	v_div_fixup_f32 v132, v180, v132, 1.0
	v_div_scale_f32 v180, s[100:101], v133, v133, 1.0
	v_rcp_f32_e32 v181, v180
	v_div_scale_f32 v182, vcc, 1.0, v133, 1.0
	v_fma_f32 v183, -v180, v181, 1.0
	v_fmac_f32_e32 v181, v183, v181
	v_mul_f32_e32 v183, v182, v181
	v_fma_f32 v184, -v180, v183, v182
	v_fmac_f32_e32 v183, v184, v181
	v_fma_f32 v180, -v180, v183, v182
	v_div_fmas_f32 v180, v180, v181, v183
	v_div_fixup_f32 v133, v180, v133, 1.0
	v_div_scale_f32 v180, s[100:101], v134, v134, 1.0
	v_rcp_f32_e32 v181, v180
	v_div_scale_f32 v182, vcc, 1.0, v134, 1.0
	v_fma_f32 v183, -v180, v181, 1.0
	v_fmac_f32_e32 v181, v183, v181
	v_mul_f32_e32 v183, v182, v181
	v_fma_f32 v184, -v180, v183, v182
	v_fmac_f32_e32 v183, v184, v181
	v_fma_f32 v180, -v180, v183, v182
	v_div_fmas_f32 v180, v180, v181, v183
	v_div_fixup_f32 v134, v180, v134, 1.0
	v_div_scale_f32 v180, s[100:101], v135, v135, 1.0
	v_rcp_f32_e32 v181, v180
	v_div_scale_f32 v182, vcc, 1.0, v135, 1.0
	v_fma_f32 v183, -v180, v181, 1.0
	v_fmac_f32_e32 v181, v183, v181
	v_mul_f32_e32 v183, v182, v181
	v_fma_f32 v184, -v180, v183, v182
	v_fmac_f32_e32 v183, v184, v181
	v_fma_f32 v180, -v180, v183, v182
	v_div_fmas_f32 v180, v180, v181, v183
	v_div_fixup_f32 v135, v180, v135, 1.0
	v_div_scale_f32 v180, s[100:101], v128, v128, 1.0
	v_rcp_f32_e32 v181, v180
	v_div_scale_f32 v182, vcc, 1.0, v128, 1.0
	v_fma_f32 v183, -v180, v181, 1.0
	v_fmac_f32_e32 v181, v183, v181
	v_mul_f32_e32 v183, v182, v181
	v_fma_f32 v184, -v180, v183, v182
	v_fmac_f32_e32 v183, v184, v181
	v_fma_f32 v180, -v180, v183, v182
	v_div_fmas_f32 v180, v180, v181, v183
	v_div_fixup_f32 v128, v180, v128, 1.0
	v_div_scale_f32 v180, s[100:101], v129, v129, 1.0
	v_rcp_f32_e32 v181, v180
	v_div_scale_f32 v182, vcc, 1.0, v129, 1.0
	v_fma_f32 v183, -v180, v181, 1.0
	v_fmac_f32_e32 v181, v183, v181
	v_mul_f32_e32 v183, v182, v181
	v_fma_f32 v184, -v180, v183, v182
	v_fmac_f32_e32 v183, v184, v181
	v_fma_f32 v180, -v180, v183, v182
	v_div_fmas_f32 v180, v180, v181, v183
	v_div_fixup_f32 v129, v180, v129, 1.0
	v_div_scale_f32 v180, s[100:101], v130, v130, 1.0
	v_rcp_f32_e32 v181, v180
	v_div_scale_f32 v182, vcc, 1.0, v130, 1.0
	v_fma_f32 v183, -v180, v181, 1.0
	v_fmac_f32_e32 v181, v183, v181
	v_mul_f32_e32 v183, v182, v181
	v_fma_f32 v184, -v180, v183, v182
	v_fmac_f32_e32 v183, v184, v181
	v_fma_f32 v180, -v180, v183, v182
	v_div_fmas_f32 v180, v180, v181, v183
	v_div_fixup_f32 v130, v180, v130, 1.0
	v_div_scale_f32 v180, s[100:101], v131, v131, 1.0
	v_rcp_f32_e32 v181, v180
	v_div_scale_f32 v182, vcc, 1.0, v131, 1.0
	v_fma_f32 v183, -v180, v181, 1.0
	v_fmac_f32_e32 v181, v183, v181
	v_mul_f32_e32 v183, v182, v181
	v_fma_f32 v184, -v180, v183, v182
	v_fmac_f32_e32 v183, v184, v181
	v_fma_f32 v180, -v180, v183, v182
	v_div_fmas_f32 v180, v180, v181, v183
	v_div_fixup_f32 v131, v180, v131, 1.0
	v_mul_f32_e32 v132, s0, v132
	v_mul_f32_e32 v133, s0, v133
	v_mul_f32_e32 v134, s0, v134
	v_mul_f32_e32 v135, s0, v135
	v_mul_f32_e32 v128, s0, v128
	v_mul_f32_e32 v129, s0, v129
	v_mul_f32_e32 v130, s0, v130
	v_mul_f32_e32 v131, s0, v131
	v_cvt_pk_bf16_f32 v188, v132, v133
	v_cvt_pk_bf16_f32 v189, v134, v135
	v_cvt_pk_bf16_f32 v190, v128, v129
	v_cvt_pk_bf16_f32 v191, v130, v131
	global_store_dwordx4 v[156:157], v[188:191], off
	v_pk_add_f32 v[124:125], v[124:125], v[164:165]
	v_pk_add_f32 v[126:127], v[126:127], v[166:167]
; __device__ __forceinline__ unsigned cvt_pk_bf16(float lo, float hi) { const f32x2c v = {lo, hi}; const bf16x2c b = __builtin_convertvector(v, bf16x2c); return __builtin_bit_cast(unsigned, b); }
; __device__ __forceinline__ float sigmoidf_(float x) { return 1.f / (1.f + __expf(-x)); }
;     __device__ __forceinline__ void operator()(const f32x4 (&acc)[2][2][4][2], const Unit& u, int wr, int wc, int fr, int fq) const {
;     ...
; #pragma unroll
;             for (int ai = 0; ai < 2; ++ai)
; #pragma unroll
;                 for (int m = 0; m < 4; ++m) { const size_t row = (size_t)(row0 + ai * HALF + m * 16);
;                     const f32x4 v0 = acc[ai][bj][m][0] + b0, v1 = acc[ai][bj][m][1] + b1; float o[8];
; #pragma unroll
;                     for (int e = 0; e < 8; ++e) { float x = (e < 4) ? v0[e & 3] : v1[e & 3];
;                         if (kind == 0) x = -0.6065306597126334f * sigmoidf_(x);
;                         else if (kind == 1) x = sigmoidf_(x);
;                         o[e] = x; }
;                     u32x4 w; w.x = cvt_pk_bf16(o[0], o[1]); w.y = cvt_pk_bf16(o[2], o[3]); w.z = cvt_pk_bf16(o[4], o[5]); w.w = cvt_pk_bf16(o[6], o[7]);
;                     *(u32x4*)(O + row * 512 + col) = w; } }
	v_pk_add_f32 v[120:121], v[120:121], v[168:169]
	v_pk_add_f32 v[122:123], v[122:123], v[170:171]
	v_mul_f32_e32 v124, 0xbfb8aa3b, v124
	v_mul_f32_e32 v125, 0xbfb8aa3b, v125
	v_mul_f32_e32 v126, 0xbfb8aa3b, v126
	v_mul_f32_e32 v127, 0xbfb8aa3b, v127
	v_mul_f32_e32 v120, 0xbfb8aa3b, v120
	v_mul_f32_e32 v121, 0xbfb8aa3b, v121
	v_mul_f32_e32 v122, 0xbfb8aa3b, v122
	v_mul_f32_e32 v123, 0xbfb8aa3b, v123
	v_exp_f32_e32 v124, v124
	v_exp_f32_e32 v125, v125
	v_exp_f32_e32 v126, v126
	v_exp_f32_e32 v127, v127
	v_exp_f32_e32 v120, v120
	v_exp_f32_e32 v121, v121
	v_exp_f32_e32 v122, v122
	v_exp_f32_e32 v123, v123
	v_pk_add_f32 v[124:125], v[124:125], 1.0 op_sel_hi:[1,0]
	v_pk_add_f32 v[126:127], v[126:127], 1.0 op_sel_hi:[1,0]
	v_pk_add_f32 v[120:121], v[120:121], 1.0 op_sel_hi:[1,0]
	v_pk_add_f32 v[122:123], v[122:123], 1.0 op_sel_hi:[1,0]
	v_div_scale_f32 v180, s[100:101], v124, v124, 1.0
	v_rcp_f32_e32 v181, v180
	v_div_scale_f32 v182, vcc, 1.0, v124, 1.0
	v_fma_f32 v183, -v180, v181, 1.0
	v_fmac_f32_e32 v181, v183, v181
	v_mul_f32_e32 v183, v182, v181
	v_fma_f32 v184, -v180, v183, v182
	v_fmac_f32_e32 v183, v184, v181
	v_fma_f32 v180, -v180, v183, v182
	v_div_fmas_f32 v180, v180, v181, v183
	v_div_fixup_f32 v124, v180, v124, 1.0
	v_div_scale_f32 v180, s[100:101], v125, v125, 1.0
	v_rcp_f32_e32 v181, v180
	v_div_scale_f32 v182, vcc, 1.0, v125, 1.0
	v_fma_f32 v183, -v180, v181, 1.0
	v_fmac_f32_e32 v181, v183, v181
	v_mul_f32_e32 v183, v182, v181
	v_fma_f32 v184, -v180, v183, v182
	v_fmac_f32_e32 v183, v184, v181
	v_fma_f32 v180, -v180, v183, v182
	v_div_fmas_f32 v180, v180, v181, v183
	v_div_fixup_f32 v125, v180, v125, 1.0
	v_div_scale_f32 v180, s[100:101], v126, v126, 1.0
	v_rcp_f32_e32 v181, v180
	v_div_scale_f32 v182, vcc, 1.0, v126, 1.0
	v_fma_f32 v183, -v180, v181, 1.0
	v_fmac_f32_e32 v181, v183, v181
	v_mul_f32_e32 v183, v182, v181
	v_fma_f32 v184, -v180, v183, v182
	v_fmac_f32_e32 v183, v184, v181
	v_fma_f32 v180, -v180, v183, v182
	v_div_fmas_f32 v180, v180, v181, v183
	v_div_fixup_f32 v126, v180, v126, 1.0
	v_div_scale_f32 v180, s[100:101], v127, v127, 1.0
	v_rcp_f32_e32 v181, v180
	v_div_scale_f32 v182, vcc, 1.0, v127, 1.0
	v_fma_f32 v183, -v180, v181, 1.0
	v_fmac_f32_e32 v181, v183, v181
	v_mul_f32_e32 v183, v182, v181
	v_fma_f32 v184, -v180, v183, v182
	v_fmac_f32_e32 v183, v184, v181
	v_fma_f32 v180, -v180, v183, v182
	v_div_fmas_f32 v180, v180, v181, v183
	v_div_fixup_f32 v127, v180, v127, 1.0
	v_div_scale_f32 v180, s[100:101], v120, v120, 1.0
	v_rcp_f32_e32 v181, v180
	v_div_scale_f32 v182, vcc, 1.0, v120, 1.0
	v_fma_f32 v183, -v180, v181, 1.0
	v_fmac_f32_e32 v181, v183, v181
	v_mul_f32_e32 v183, v182, v181
	v_fma_f32 v184, -v180, v183, v182
	v_fmac_f32_e32 v183, v184, v181
	v_fma_f32 v180, -v180, v183, v182
	v_div_fmas_f32 v180, v180, v181, v183
	v_div_fixup_f32 v120, v180, v120, 1.0
	v_div_scale_f32 v180, s[100:101], v121, v121, 1.0
	v_rcp_f32_e32 v181, v180
	v_div_scale_f32 v182, vcc, 1.0, v121, 1.0
	v_fma_f32 v183, -v180, v181, 1.0
	v_fmac_f32_e32 v181, v183, v181
	v_mul_f32_e32 v183, v182, v181
	v_fma_f32 v184, -v180, v183, v182
	v_fmac_f32_e32 v183, v184, v181
	v_fma_f32 v180, -v180, v183, v182
	v_div_fmas_f32 v180, v180, v181, v183
	v_div_fixup_f32 v121, v180, v121, 1.0
	v_div_scale_f32 v180, s[100:101], v122, v122, 1.0
	v_rcp_f32_e32 v181, v180
	v_div_scale_f32 v182, vcc, 1.0, v122, 1.0
	v_fma_f32 v183, -v180, v181, 1.0
	v_fmac_f32_e32 v181, v183, v181
	v_mul_f32_e32 v183, v182, v181
	v_fma_f32 v184, -v180, v183, v182
	v_fmac_f32_e32 v183, v184, v181
	v_fma_f32 v180, -v180, v183, v182
	v_div_fmas_f32 v180, v180, v181, v183
	v_div_fixup_f32 v122, v180, v122, 1.0
	v_div_scale_f32 v180, s[100:101], v123, v123, 1.0
	v_rcp_f32_e32 v181, v180
	v_div_scale_f32 v182, vcc, 1.0, v123, 1.0
	v_fma_f32 v183, -v180, v181, 1.0
	v_fmac_f32_e32 v181, v183, v181
	v_mul_f32_e32 v183, v182, v181
	v_fma_f32 v184, -v180, v183, v182
	v_fmac_f32_e32 v183, v184, v181
	v_fma_f32 v180, -v180, v183, v182
	v_div_fmas_f32 v180, v180, v181, v183
	v_div_fixup_f32 v123, v180, v123, 1.0
	v_mul_f32_e32 v124, s0, v124
	v_mul_f32_e32 v125, s0, v125
	v_mul_f32_e32 v126, s0, v126
	v_mul_f32_e32 v127, s0, v127
	v_mul_f32_e32 v120, s0, v120
	v_mul_f32_e32 v121, s0, v121
	v_mul_f32_e32 v122, s0, v122
	v_mul_f32_e32 v123, s0, v123
	s_mov_b64 s[98:99], 0x4000
	v_lshl_add_u64 v[158:159], v[156:157], 0, s[98:99]
	v_cvt_pk_bf16_f32 v192, v124, v125
	v_cvt_pk_bf16_f32 v193, v126, v127
	v_cvt_pk_bf16_f32 v194, v120, v121
	v_cvt_pk_bf16_f32 v195, v122, v123
	global_store_dwordx4 v[158:159], v[192:195], off
	v_pk_add_f32 v[116:117], v[116:117], v[164:165]
	v_pk_add_f32 v[118:119], v[118:119], v[166:167]
	v_pk_add_f32 v[112:113], v[112:113], v[168:169]
	v_pk_add_f32 v[114:115], v[114:115], v[170:171]
	v_mul_f32_e32 v116, 0xbfb8aa3b, v116
	v_mul_f32_e32 v117, 0xbfb8aa3b, v117
	v_mul_f32_e32 v118, 0xbfb8aa3b, v118
	v_mul_f32_e32 v119, 0xbfb8aa3b, v119
	v_mul_f32_e32 v112, 0xbfb8aa3b, v112
	v_mul_f32_e32 v113, 0xbfb8aa3b, v113
	v_mul_f32_e32 v114, 0xbfb8aa3b, v114
	v_mul_f32_e32 v115, 0xbfb8aa3b, v115
	v_exp_f32_e32 v116, v116
	v_exp_f32_e32 v117, v117
	v_exp_f32_e32 v118, v118
	v_exp_f32_e32 v119, v119
	v_exp_f32_e32 v112, v112
	v_exp_f32_e32 v113, v113
	v_exp_f32_e32 v114, v114
	v_exp_f32_e32 v115, v115
	v_pk_add_f32 v[116:117], v[116:117], 1.0 op_sel_hi:[1,0]
	v_pk_add_f32 v[118:119], v[118:119], 1.0 op_sel_hi:[1,0]
	v_pk_add_f32 v[112:113], v[112:113], 1.0 op_sel_hi:[1,0]
	v_pk_add_f32 v[114:115], v[114:115], 1.0 op_sel_hi:[1,0]
	v_div_scale_f32 v180, s[100:101], v116, v116, 1.0
	v_rcp_f32_e32 v181, v180
	v_div_scale_f32 v182, vcc, 1.0, v116, 1.0
	v_fma_f32 v183, -v180, v181, 1.0
; __device__ __forceinline__ unsigned cvt_pk_bf16(float lo, float hi) { const f32x2c v = {lo, hi}; const bf16x2c b = __builtin_convertvector(v, bf16x2c); return __builtin_bit_cast(unsigned, b); }
; __device__ __forceinline__ float sigmoidf_(float x) { return 1.f / (1.f + __expf(-x)); }
;     __device__ __forceinline__ void operator()(const f32x4 (&acc)[2][2][4][2], const Unit& u, int wr, int wc, int fr, int fq) const {
;     ...
; #pragma unroll
;             for (int ai = 0; ai < 2; ++ai)
; #pragma unroll
;                 for (int m = 0; m < 4; ++m) { const size_t row = (size_t)(row0 + ai * HALF + m * 16);
;                     const f32x4 v0 = acc[ai][bj][m][0] + b0, v1 = acc[ai][bj][m][1] + b1; float o[8];
; #pragma unroll
;                     for (int e = 0; e < 8; ++e) { float x = (e < 4) ? v0[e & 3] : v1[e & 3];
;                         if (kind == 0) x = -0.6065306597126334f * sigmoidf_(x);
;                         else if (kind == 1) x = sigmoidf_(x);
;                         o[e] = x; }
;                     u32x4 w; w.x = cvt_pk_bf16(o[0], o[1]); w.y = cvt_pk_bf16(o[2], o[3]); w.z = cvt_pk_bf16(o[4], o[5]); w.w = cvt_pk_bf16(o[6], o[7]);
;                     *(u32x4*)(O + row * 512 + col) = w; } }
	v_fmac_f32_e32 v181, v183, v181
	v_mul_f32_e32 v183, v182, v181
	v_fma_f32 v184, -v180, v183, v182
	v_fmac_f32_e32 v183, v184, v181
	v_fma_f32 v180, -v180, v183, v182
	v_div_fmas_f32 v180, v180, v181, v183
	v_div_fixup_f32 v116, v180, v116, 1.0
	v_div_scale_f32 v180, s[100:101], v117, v117, 1.0
	v_rcp_f32_e32 v181, v180
	v_div_scale_f32 v182, vcc, 1.0, v117, 1.0
	v_fma_f32 v183, -v180, v181, 1.0
	v_fmac_f32_e32 v181, v183, v181
	v_mul_f32_e32 v183, v182, v181
	v_fma_f32 v184, -v180, v183, v182
	v_fmac_f32_e32 v183, v184, v181
	v_fma_f32 v180, -v180, v183, v182
	v_div_fmas_f32 v180, v180, v181, v183
	v_div_fixup_f32 v117, v180, v117, 1.0
	v_div_scale_f32 v180, s[100:101], v118, v118, 1.0
	v_rcp_f32_e32 v181, v180
	v_div_scale_f32 v182, vcc, 1.0, v118, 1.0
	v_fma_f32 v183, -v180, v181, 1.0
	v_fmac_f32_e32 v181, v183, v181
	v_mul_f32_e32 v183, v182, v181
	v_fma_f32 v184, -v180, v183, v182
	v_fmac_f32_e32 v183, v184, v181
	v_fma_f32 v180, -v180, v183, v182
	v_div_fmas_f32 v180, v180, v181, v183
	v_div_fixup_f32 v118, v180, v118, 1.0
	v_div_scale_f32 v180, s[100:101], v119, v119, 1.0
	v_rcp_f32_e32 v181, v180
	v_div_scale_f32 v182, vcc, 1.0, v119, 1.0
	v_fma_f32 v183, -v180, v181, 1.0
	v_fmac_f32_e32 v181, v183, v181
	v_mul_f32_e32 v183, v182, v181
	v_fma_f32 v184, -v180, v183, v182
	v_fmac_f32_e32 v183, v184, v181
	v_fma_f32 v180, -v180, v183, v182
	v_div_fmas_f32 v180, v180, v181, v183
	v_div_fixup_f32 v119, v180, v119, 1.0
	v_div_scale_f32 v180, s[100:101], v112, v112, 1.0
	v_rcp_f32_e32 v181, v180
	v_div_scale_f32 v182, vcc, 1.0, v112, 1.0
	v_fma_f32 v183, -v180, v181, 1.0
	v_fmac_f32_e32 v181, v183, v181
	v_mul_f32_e32 v183, v182, v181
	v_fma_f32 v184, -v180, v183, v182
	v_fmac_f32_e32 v183, v184, v181
	v_fma_f32 v180, -v180, v183, v182
	v_div_fmas_f32 v180, v180, v181, v183
	v_div_fixup_f32 v112, v180, v112, 1.0
	v_div_scale_f32 v180, s[100:101], v113, v113, 1.0
	v_rcp_f32_e32 v181, v180
	v_div_scale_f32 v182, vcc, 1.0, v113, 1.0
	v_fma_f32 v183, -v180, v181, 1.0
	v_fmac_f32_e32 v181, v183, v181
	v_mul_f32_e32 v183, v182, v181
	v_fma_f32 v184, -v180, v183, v182
	v_fmac_f32_e32 v183, v184, v181
	v_fma_f32 v180, -v180, v183, v182
	v_div_fmas_f32 v180, v180, v181, v183
	v_div_fixup_f32 v113, v180, v113, 1.0
	v_div_scale_f32 v180, s[100:101], v114, v114, 1.0
	v_rcp_f32_e32 v181, v180
	v_div_scale_f32 v182, vcc, 1.0, v114, 1.0
	v_fma_f32 v183, -v180, v181, 1.0
	v_fmac_f32_e32 v181, v183, v181
	v_mul_f32_e32 v183, v182, v181
	v_fma_f32 v184, -v180, v183, v182
	v_fmac_f32_e32 v183, v184, v181
	v_fma_f32 v180, -v180, v183, v182
	v_div_fmas_f32 v180, v180, v181, v183
	v_div_fixup_f32 v114, v180, v114, 1.0
	v_div_scale_f32 v180, s[100:101], v115, v115, 1.0
	v_rcp_f32_e32 v181, v180
	v_div_scale_f32 v182, vcc, 1.0, v115, 1.0
	v_fma_f32 v183, -v180, v181, 1.0
	v_fmac_f32_e32 v181, v183, v181
	v_mul_f32_e32 v183, v182, v181
	v_fma_f32 v184, -v180, v183, v182
	v_fmac_f32_e32 v183, v184, v181
	v_fma_f32 v180, -v180, v183, v182
	v_div_fmas_f32 v180, v180, v181, v183
	v_div_fixup_f32 v115, v180, v115, 1.0
	v_mul_f32_e32 v116, s0, v116
	v_mul_f32_e32 v117, s0, v117
	v_mul_f32_e32 v118, s0, v118
	v_mul_f32_e32 v119, s0, v119
	v_mul_f32_e32 v112, s0, v112
	v_mul_f32_e32 v113, s0, v113
	v_mul_f32_e32 v114, s0, v114
	v_mul_f32_e32 v115, s0, v115
	s_mov_b64 s[98:99], 0x8000
	v_lshl_add_u64 v[158:159], v[156:157], 0, s[98:99]
	v_cvt_pk_bf16_f32 v188, v116, v117
	v_cvt_pk_bf16_f32 v189, v118, v119
	v_cvt_pk_bf16_f32 v190, v112, v113
	v_cvt_pk_bf16_f32 v191, v114, v115
	global_store_dwordx4 v[158:159], v[188:191], off
	v_pk_add_f32 v[108:109], v[108:109], v[164:165]
	v_pk_add_f32 v[110:111], v[110:111], v[166:167]
	v_pk_add_f32 v[104:105], v[104:105], v[168:169]
	v_pk_add_f32 v[106:107], v[106:107], v[170:171]
	v_mul_f32_e32 v108, 0xbfb8aa3b, v108
	v_mul_f32_e32 v109, 0xbfb8aa3b, v109
	v_mul_f32_e32 v110, 0xbfb8aa3b, v110
	v_mul_f32_e32 v111, 0xbfb8aa3b, v111
	v_mul_f32_e32 v104, 0xbfb8aa3b, v104
	v_mul_f32_e32 v105, 0xbfb8aa3b, v105
	v_mul_f32_e32 v106, 0xbfb8aa3b, v106
	v_mul_f32_e32 v107, 0xbfb8aa3b, v107
	v_exp_f32_e32 v108, v108
	v_exp_f32_e32 v109, v109
	v_exp_f32_e32 v110, v110
	v_exp_f32_e32 v111, v111
	v_exp_f32_e32 v104, v104
	v_exp_f32_e32 v105, v105
	v_exp_f32_e32 v106, v106
	v_exp_f32_e32 v107, v107
	v_pk_add_f32 v[108:109], v[108:109], 1.0 op_sel_hi:[1,0]
	v_pk_add_f32 v[110:111], v[110:111], 1.0 op_sel_hi:[1,0]
	v_pk_add_f32 v[104:105], v[104:105], 1.0 op_sel_hi:[1,0]
	v_pk_add_f32 v[106:107], v[106:107], 1.0 op_sel_hi:[1,0]
	v_div_scale_f32 v180, s[100:101], v108, v108, 1.0
	v_rcp_f32_e32 v181, v180
	v_div_scale_f32 v182, vcc, 1.0, v108, 1.0
	v_fma_f32 v183, -v180, v181, 1.0
	v_fmac_f32_e32 v181, v183, v181
	v_mul_f32_e32 v183, v182, v181
	v_fma_f32 v184, -v180, v183, v182
	v_fmac_f32_e32 v183, v184, v181
	v_fma_f32 v180, -v180, v183, v182
	v_div_fmas_f32 v180, v180, v181, v183
	v_div_fixup_f32 v108, v180, v108, 1.0
	v_div_scale_f32 v180, s[100:101], v109, v109, 1.0
	v_rcp_f32_e32 v181, v180
	v_div_scale_f32 v182, vcc, 1.0, v109, 1.0
	v_fma_f32 v183, -v180, v181, 1.0
	v_fmac_f32_e32 v181, v183, v181
	v_mul_f32_e32 v183, v182, v181
	v_fma_f32 v184, -v180, v183, v182
	v_fmac_f32_e32 v183, v184, v181
	v_fma_f32 v180, -v180, v183, v182
	v_div_fmas_f32 v180, v180, v181, v183
	v_div_fixup_f32 v109, v180, v109, 1.0
	v_div_scale_f32 v180, s[100:101], v110, v110, 1.0
	v_rcp_f32_e32 v181, v180
	v_div_scale_f32 v182, vcc, 1.0, v110, 1.0
	v_fma_f32 v183, -v180, v181, 1.0
	v_fmac_f32_e32 v181, v183, v181
	v_mul_f32_e32 v183, v182, v181
	v_fma_f32 v184, -v180, v183, v182
	v_fmac_f32_e32 v183, v184, v181
	v_fma_f32 v180, -v180, v183, v182
; __device__ __forceinline__ unsigned cvt_pk_bf16(float lo, float hi) { const f32x2c v = {lo, hi}; const bf16x2c b = __builtin_convertvector(v, bf16x2c); return __builtin_bit_cast(unsigned, b); }
; __device__ __forceinline__ float sigmoidf_(float x) { return 1.f / (1.f + __expf(-x)); }
;     __device__ __forceinline__ void operator()(const f32x4 (&acc)[2][2][4][2], const Unit& u, int wr, int wc, int fr, int fq) const {
;     ...
; #pragma unroll
;             for (int ai = 0; ai < 2; ++ai)
; #pragma unroll
;                 for (int m = 0; m < 4; ++m) { const size_t row = (size_t)(row0 + ai * HALF + m * 16);
;                     const f32x4 v0 = acc[ai][bj][m][0] + b0, v1 = acc[ai][bj][m][1] + b1; float o[8];
; #pragma unroll
;                     for (int e = 0; e < 8; ++e) { float x = (e < 4) ? v0[e & 3] : v1[e & 3];
;                         if (kind == 0) x = -0.6065306597126334f * sigmoidf_(x);
;                         else if (kind == 1) x = sigmoidf_(x);
;                         o[e] = x; }
;                     u32x4 w; w.x = cvt_pk_bf16(o[0], o[1]); w.y = cvt_pk_bf16(o[2], o[3]); w.z = cvt_pk_bf16(o[4], o[5]); w.w = cvt_pk_bf16(o[6], o[7]);
;                     *(u32x4*)(O + row * 512 + col) = w; } }
	v_div_fmas_f32 v180, v180, v181, v183
	v_div_fixup_f32 v110, v180, v110, 1.0
	v_div_scale_f32 v180, s[100:101], v111, v111, 1.0
	v_rcp_f32_e32 v181, v180
	v_div_scale_f32 v182, vcc, 1.0, v111, 1.0
	v_fma_f32 v183, -v180, v181, 1.0
	v_fmac_f32_e32 v181, v183, v181
	v_mul_f32_e32 v183, v182, v181
	v_fma_f32 v184, -v180, v183, v182
	v_fmac_f32_e32 v183, v184, v181
	v_fma_f32 v180, -v180, v183, v182
	v_div_fmas_f32 v180, v180, v181, v183
	v_div_fixup_f32 v111, v180, v111, 1.0
	v_div_scale_f32 v180, s[100:101], v104, v104, 1.0
	v_rcp_f32_e32 v181, v180
	v_div_scale_f32 v182, vcc, 1.0, v104, 1.0
	v_fma_f32 v183, -v180, v181, 1.0
	v_fmac_f32_e32 v181, v183, v181
	v_mul_f32_e32 v183, v182, v181
	v_fma_f32 v184, -v180, v183, v182
	v_fmac_f32_e32 v183, v184, v181
	v_fma_f32 v180, -v180, v183, v182
	v_div_fmas_f32 v180, v180, v181, v183
	v_div_fixup_f32 v104, v180, v104, 1.0
	v_div_scale_f32 v180, s[100:101], v105, v105, 1.0
	v_rcp_f32_e32 v181, v180
	v_div_scale_f32 v182, vcc, 1.0, v105, 1.0
	v_fma_f32 v183, -v180, v181, 1.0
	v_fmac_f32_e32 v181, v183, v181
	v_mul_f32_e32 v183, v182, v181
	v_fma_f32 v184, -v180, v183, v182
	v_fmac_f32_e32 v183, v184, v181
	v_fma_f32 v180, -v180, v183, v182
	v_div_fmas_f32 v180, v180, v181, v183
	v_div_fixup_f32 v105, v180, v105, 1.0
	v_div_scale_f32 v180, s[100:101], v106, v106, 1.0
	v_rcp_f32_e32 v181, v180
	v_div_scale_f32 v182, vcc, 1.0, v106, 1.0
	v_fma_f32 v183, -v180, v181, 1.0
	v_fmac_f32_e32 v181, v183, v181
	v_mul_f32_e32 v183, v182, v181
	v_fma_f32 v184, -v180, v183, v182
	v_fmac_f32_e32 v183, v184, v181
	v_fma_f32 v180, -v180, v183, v182
	v_div_fmas_f32 v180, v180, v181, v183
	v_div_fixup_f32 v106, v180, v106, 1.0
	v_div_scale_f32 v180, s[100:101], v107, v107, 1.0
	v_rcp_f32_e32 v181, v180
	v_div_scale_f32 v182, vcc, 1.0, v107, 1.0
	v_fma_f32 v183, -v180, v181, 1.0
	v_fmac_f32_e32 v181, v183, v181
	v_mul_f32_e32 v183, v182, v181
	v_fma_f32 v184, -v180, v183, v182
	v_fmac_f32_e32 v183, v184, v181
	v_fma_f32 v180, -v180, v183, v182
	v_div_fmas_f32 v180, v180, v181, v183
	v_div_fixup_f32 v107, v180, v107, 1.0
	v_mul_f32_e32 v108, s0, v108
	v_mul_f32_e32 v109, s0, v109
	v_mul_f32_e32 v110, s0, v110
	v_mul_f32_e32 v111, s0, v111
	v_mul_f32_e32 v104, s0, v104
	v_mul_f32_e32 v105, s0, v105
	v_mul_f32_e32 v106, s0, v106
	v_mul_f32_e32 v107, s0, v107
	s_mov_b64 s[98:99], 0xc000
	v_lshl_add_u64 v[158:159], v[156:157], 0, s[98:99]
	v_cvt_pk_bf16_f32 v192, v108, v109
	v_cvt_pk_bf16_f32 v193, v110, v111
	v_cvt_pk_bf16_f32 v194, v104, v105
	v_cvt_pk_bf16_f32 v195, v106, v107
	global_store_dwordx4 v[158:159], v[192:195], off
	v_pk_add_f32 v[100:101], v[100:101], v[164:165]
	v_pk_add_f32 v[102:103], v[102:103], v[166:167]
	v_pk_add_f32 v[96:97], v[96:97], v[168:169]
	v_pk_add_f32 v[98:99], v[98:99], v[170:171]
	v_mul_f32_e32 v100, 0xbfb8aa3b, v100
	v_mul_f32_e32 v101, 0xbfb8aa3b, v101
	v_mul_f32_e32 v102, 0xbfb8aa3b, v102
	v_mul_f32_e32 v103, 0xbfb8aa3b, v103
	v_mul_f32_e32 v96, 0xbfb8aa3b, v96
	v_mul_f32_e32 v97, 0xbfb8aa3b, v97
	v_mul_f32_e32 v98, 0xbfb8aa3b, v98
	v_mul_f32_e32 v99, 0xbfb8aa3b, v99
	v_exp_f32_e32 v100, v100
	v_exp_f32_e32 v101, v101
	v_exp_f32_e32 v102, v102
	v_exp_f32_e32 v103, v103
	v_exp_f32_e32 v96, v96
	v_exp_f32_e32 v97, v97
	v_exp_f32_e32 v98, v98
	v_exp_f32_e32 v99, v99
	v_pk_add_f32 v[100:101], v[100:101], 1.0 op_sel_hi:[1,0]
	v_pk_add_f32 v[102:103], v[102:103], 1.0 op_sel_hi:[1,0]
	v_pk_add_f32 v[96:97], v[96:97], 1.0 op_sel_hi:[1,0]
	v_pk_add_f32 v[98:99], v[98:99], 1.0 op_sel_hi:[1,0]
	v_div_scale_f32 v180, s[100:101], v100, v100, 1.0
	v_rcp_f32_e32 v181, v180
	v_div_scale_f32 v182, vcc, 1.0, v100, 1.0
	v_fma_f32 v183, -v180, v181, 1.0
	v_fmac_f32_e32 v181, v183, v181
	v_mul_f32_e32 v183, v182, v181
	v_fma_f32 v184, -v180, v183, v182
	v_fmac_f32_e32 v183, v184, v181
	v_fma_f32 v180, -v180, v183, v182
	v_div_fmas_f32 v180, v180, v181, v183
	v_div_fixup_f32 v100, v180, v100, 1.0
	v_div_scale_f32 v180, s[100:101], v101, v101, 1.0
	v_rcp_f32_e32 v181, v180
	v_div_scale_f32 v182, vcc, 1.0, v101, 1.0
	v_fma_f32 v183, -v180, v181, 1.0
	v_fmac_f32_e32 v181, v183, v181
	v_mul_f32_e32 v183, v182, v181
	v_fma_f32 v184, -v180, v183, v182
	v_fmac_f32_e32 v183, v184, v181
	v_fma_f32 v180, -v180, v183, v182
	v_div_fmas_f32 v180, v180, v181, v183
	v_div_fixup_f32 v101, v180, v101, 1.0
	v_div_scale_f32 v180, s[100:101], v102, v102, 1.0
	v_rcp_f32_e32 v181, v180
	v_div_scale_f32 v182, vcc, 1.0, v102, 1.0
	v_fma_f32 v183, -v180, v181, 1.0
	v_fmac_f32_e32 v181, v183, v181
	v_mul_f32_e32 v183, v182, v181
	v_fma_f32 v184, -v180, v183, v182
	v_fmac_f32_e32 v183, v184, v181
	v_fma_f32 v180, -v180, v183, v182
	v_div_fmas_f32 v180, v180, v181, v183
	v_div_fixup_f32 v102, v180, v102, 1.0
	v_div_scale_f32 v180, s[100:101], v103, v103, 1.0
	v_rcp_f32_e32 v181, v180
	v_div_scale_f32 v182, vcc, 1.0, v103, 1.0
	v_fma_f32 v183, -v180, v181, 1.0
	v_fmac_f32_e32 v181, v183, v181
	v_mul_f32_e32 v183, v182, v181
	v_fma_f32 v184, -v180, v183, v182
	v_fmac_f32_e32 v183, v184, v181
	v_fma_f32 v180, -v180, v183, v182
	v_div_fmas_f32 v180, v180, v181, v183
	v_div_fixup_f32 v103, v180, v103, 1.0
	v_div_scale_f32 v180, s[100:101], v96, v96, 1.0
	v_rcp_f32_e32 v181, v180
	v_div_scale_f32 v182, vcc, 1.0, v96, 1.0
	v_fma_f32 v183, -v180, v181, 1.0
	v_fmac_f32_e32 v181, v183, v181
	v_mul_f32_e32 v183, v182, v181
	v_fma_f32 v184, -v180, v183, v182
	v_fmac_f32_e32 v183, v184, v181
	v_fma_f32 v180, -v180, v183, v182
	v_div_fmas_f32 v180, v180, v181, v183
	v_div_fixup_f32 v96, v180, v96, 1.0
	v_div_scale_f32 v180, s[100:101], v97, v97, 1.0
	v_rcp_f32_e32 v181, v180
	v_div_scale_f32 v182, vcc, 1.0, v97, 1.0
	v_fma_f32 v183, -v180, v181, 1.0
; __device__ __forceinline__ unsigned cvt_pk_bf16(float lo, float hi) { const f32x2c v = {lo, hi}; const bf16x2c b = __builtin_convertvector(v, bf16x2c); return __builtin_bit_cast(unsigned, b); }
; __device__ __forceinline__ float sigmoidf_(float x) { return 1.f / (1.f + __expf(-x)); }
;     __device__ __forceinline__ void operator()(const f32x4 (&acc)[2][2][4][2], const Unit& u, int wr, int wc, int fr, int fq) const {
;     ...
; #pragma unroll
;             for (int ai = 0; ai < 2; ++ai)
; #pragma unroll
;                 for (int m = 0; m < 4; ++m) { const size_t row = (size_t)(row0 + ai * HALF + m * 16);
;                     const f32x4 v0 = acc[ai][bj][m][0] + b0, v1 = acc[ai][bj][m][1] + b1; float o[8];
; #pragma unroll
;                     for (int e = 0; e < 8; ++e) { float x = (e < 4) ? v0[e & 3] : v1[e & 3];
;                         if (kind == 0) x = -0.6065306597126334f * sigmoidf_(x);
;                         else if (kind == 1) x = sigmoidf_(x);
;                         o[e] = x; }
;                     u32x4 w; w.x = cvt_pk_bf16(o[0], o[1]); w.y = cvt_pk_bf16(o[2], o[3]); w.z = cvt_pk_bf16(o[4], o[5]); w.w = cvt_pk_bf16(o[6], o[7]);
;                     *(u32x4*)(O + row * 512 + col) = w; } }
	v_fmac_f32_e32 v181, v183, v181
	v_mul_f32_e32 v183, v182, v181
	v_fma_f32 v184, -v180, v183, v182
	v_fmac_f32_e32 v183, v184, v181
	v_fma_f32 v180, -v180, v183, v182
	v_div_fmas_f32 v180, v180, v181, v183
	v_div_fixup_f32 v97, v180, v97, 1.0
	v_div_scale_f32 v180, s[100:101], v98, v98, 1.0
	v_rcp_f32_e32 v181, v180
	v_div_scale_f32 v182, vcc, 1.0, v98, 1.0
	v_fma_f32 v183, -v180, v181, 1.0
	v_fmac_f32_e32 v181, v183, v181
	v_mul_f32_e32 v183, v182, v181
	v_fma_f32 v184, -v180, v183, v182
	v_fmac_f32_e32 v183, v184, v181
	v_fma_f32 v180, -v180, v183, v182
	v_div_fmas_f32 v180, v180, v181, v183
	v_div_fixup_f32 v98, v180, v98, 1.0
	v_div_scale_f32 v180, s[100:101], v99, v99, 1.0
	v_rcp_f32_e32 v181, v180
	v_div_scale_f32 v182, vcc, 1.0, v99, 1.0
	v_fma_f32 v183, -v180, v181, 1.0
	v_fmac_f32_e32 v181, v183, v181
	v_mul_f32_e32 v183, v182, v181
	v_fma_f32 v184, -v180, v183, v182
	v_fmac_f32_e32 v183, v184, v181
	v_fma_f32 v180, -v180, v183, v182
	v_div_fmas_f32 v180, v180, v181, v183
	v_div_fixup_f32 v99, v180, v99, 1.0
	v_mul_f32_e32 v100, s0, v100
	v_mul_f32_e32 v101, s0, v101
	v_mul_f32_e32 v102, s0, v102
	v_mul_f32_e32 v103, s0, v103
	v_mul_f32_e32 v96, s0, v96
	v_mul_f32_e32 v97, s0, v97
	v_mul_f32_e32 v98, s0, v98
	v_mul_f32_e32 v99, s0, v99
	s_mov_b64 s[98:99], 0x20000
	v_lshl_add_u64 v[158:159], v[156:157], 0, s[98:99]
	v_cvt_pk_bf16_f32 v188, v100, v101
	v_cvt_pk_bf16_f32 v189, v102, v103
	v_cvt_pk_bf16_f32 v190, v96, v97
	v_cvt_pk_bf16_f32 v191, v98, v99
	global_store_dwordx4 v[158:159], v[188:191], off
	v_pk_add_f32 v[92:93], v[92:93], v[164:165]
	v_pk_add_f32 v[94:95], v[94:95], v[166:167]
	v_pk_add_f32 v[84:85], v[84:85], v[168:169]
	v_pk_add_f32 v[86:87], v[86:87], v[170:171]
	v_mul_f32_e32 v92, 0xbfb8aa3b, v92
	v_mul_f32_e32 v93, 0xbfb8aa3b, v93
	v_mul_f32_e32 v94, 0xbfb8aa3b, v94
	v_mul_f32_e32 v95, 0xbfb8aa3b, v95
	v_mul_f32_e32 v84, 0xbfb8aa3b, v84
	v_mul_f32_e32 v85, 0xbfb8aa3b, v85
	v_mul_f32_e32 v86, 0xbfb8aa3b, v86
	v_mul_f32_e32 v87, 0xbfb8aa3b, v87
	v_exp_f32_e32 v92, v92
	v_exp_f32_e32 v93, v93
	v_exp_f32_e32 v94, v94
	v_exp_f32_e32 v95, v95
	v_exp_f32_e32 v84, v84
	v_exp_f32_e32 v85, v85
	v_exp_f32_e32 v86, v86
	v_exp_f32_e32 v87, v87
	v_pk_add_f32 v[92:93], v[92:93], 1.0 op_sel_hi:[1,0]
	v_pk_add_f32 v[94:95], v[94:95], 1.0 op_sel_hi:[1,0]
	v_pk_add_f32 v[84:85], v[84:85], 1.0 op_sel_hi:[1,0]
	v_pk_add_f32 v[86:87], v[86:87], 1.0 op_sel_hi:[1,0]
	v_div_scale_f32 v180, s[100:101], v92, v92, 1.0
	v_rcp_f32_e32 v181, v180
	v_div_scale_f32 v182, vcc, 1.0, v92, 1.0
	v_fma_f32 v183, -v180, v181, 1.0
	v_fmac_f32_e32 v181, v183, v181
	v_mul_f32_e32 v183, v182, v181
	v_fma_f32 v184, -v180, v183, v182
	v_fmac_f32_e32 v183, v184, v181
	v_fma_f32 v180, -v180, v183, v182
	v_div_fmas_f32 v180, v180, v181, v183
	v_div_fixup_f32 v92, v180, v92, 1.0
	v_div_scale_f32 v180, s[100:101], v93, v93, 1.0
	v_rcp_f32_e32 v181, v180
	v_div_scale_f32 v182, vcc, 1.0, v93, 1.0
	v_fma_f32 v183, -v180, v181, 1.0
	v_fmac_f32_e32 v181, v183, v181
	v_mul_f32_e32 v183, v182, v181
	v_fma_f32 v184, -v180, v183, v182
	v_fmac_f32_e32 v183, v184, v181
	v_fma_f32 v180, -v180, v183, v182
	v_div_fmas_f32 v180, v180, v181, v183
	v_div_fixup_f32 v93, v180, v93, 1.0
	v_div_scale_f32 v180, s[100:101], v94, v94, 1.0
	v_rcp_f32_e32 v181, v180
	v_div_scale_f32 v182, vcc, 1.0, v94, 1.0
	v_fma_f32 v183, -v180, v181, 1.0
	v_fmac_f32_e32 v181, v183, v181
	v_mul_f32_e32 v183, v182, v181
	v_fma_f32 v184, -v180, v183, v182
	v_fmac_f32_e32 v183, v184, v181
	v_fma_f32 v180, -v180, v183, v182
	v_div_fmas_f32 v180, v180, v181, v183
	v_div_fixup_f32 v94, v180, v94, 1.0
	v_div_scale_f32 v180, s[100:101], v95, v95, 1.0
	v_rcp_f32_e32 v181, v180
	v_div_scale_f32 v182, vcc, 1.0, v95, 1.0
	v_fma_f32 v183, -v180, v181, 1.0
	v_fmac_f32_e32 v181, v183, v181
	v_mul_f32_e32 v183, v182, v181
	v_fma_f32 v184, -v180, v183, v182
	v_fmac_f32_e32 v183, v184, v181
	v_fma_f32 v180, -v180, v183, v182
	v_div_fmas_f32 v180, v180, v181, v183
	v_div_fixup_f32 v95, v180, v95, 1.0
	v_div_scale_f32 v180, s[100:101], v84, v84, 1.0
	v_rcp_f32_e32 v181, v180
	v_div_scale_f32 v182, vcc, 1.0, v84, 1.0
	v_fma_f32 v183, -v180, v181, 1.0
	v_fmac_f32_e32 v181, v183, v181
	v_mul_f32_e32 v183, v182, v181
	v_fma_f32 v184, -v180, v183, v182
	v_fmac_f32_e32 v183, v184, v181
	v_fma_f32 v180, -v180, v183, v182
	v_div_fmas_f32 v180, v180, v181, v183
	v_div_fixup_f32 v84, v180, v84, 1.0
	v_div_scale_f32 v180, s[100:101], v85, v85, 1.0
	v_rcp_f32_e32 v181, v180
	v_div_scale_f32 v182, vcc, 1.0, v85, 1.0
	v_fma_f32 v183, -v180, v181, 1.0
	v_fmac_f32_e32 v181, v183, v181
	v_mul_f32_e32 v183, v182, v181
	v_fma_f32 v184, -v180, v183, v182
	v_fmac_f32_e32 v183, v184, v181
	v_fma_f32 v180, -v180, v183, v182
	v_div_fmas_f32 v180, v180, v181, v183
	v_div_fixup_f32 v85, v180, v85, 1.0
	v_div_scale_f32 v180, s[100:101], v86, v86, 1.0
	v_rcp_f32_e32 v181, v180
	v_div_scale_f32 v182, vcc, 1.0, v86, 1.0
	v_fma_f32 v183, -v180, v181, 1.0
	v_fmac_f32_e32 v181, v183, v181
	v_mul_f32_e32 v183, v182, v181
	v_fma_f32 v184, -v180, v183, v182
	v_fmac_f32_e32 v183, v184, v181
	v_fma_f32 v180, -v180, v183, v182
	v_div_fmas_f32 v180, v180, v181, v183
	v_div_fixup_f32 v86, v180, v86, 1.0
	v_div_scale_f32 v180, s[100:101], v87, v87, 1.0
	v_rcp_f32_e32 v181, v180
	v_div_scale_f32 v182, vcc, 1.0, v87, 1.0
	v_fma_f32 v183, -v180, v181, 1.0
	v_fmac_f32_e32 v181, v183, v181
	v_mul_f32_e32 v183, v182, v181
	v_fma_f32 v184, -v180, v183, v182
	v_fmac_f32_e32 v183, v184, v181
	v_fma_f32 v180, -v180, v183, v182
	v_div_fmas_f32 v180, v180, v181, v183
	v_div_fixup_f32 v87, v180, v87, 1.0
	v_mul_f32_e32 v92, s0, v92
	v_mul_f32_e32 v93, s0, v93
; __device__ __forceinline__ unsigned cvt_pk_bf16(float lo, float hi) { const f32x2c v = {lo, hi}; const bf16x2c b = __builtin_convertvector(v, bf16x2c); return __builtin_bit_cast(unsigned, b); }
; __device__ __forceinline__ float sigmoidf_(float x) { return 1.f / (1.f + __expf(-x)); }
;     __device__ __forceinline__ void operator()(const f32x4 (&acc)[2][2][4][2], const Unit& u, int wr, int wc, int fr, int fq) const {
;     ...
; #pragma unroll
;             for (int ai = 0; ai < 2; ++ai)
; #pragma unroll
;                 for (int m = 0; m < 4; ++m) { const size_t row = (size_t)(row0 + ai * HALF + m * 16);
;                     const f32x4 v0 = acc[ai][bj][m][0] + b0, v1 = acc[ai][bj][m][1] + b1; float o[8];
; #pragma unroll
;                     for (int e = 0; e < 8; ++e) { float x = (e < 4) ? v0[e & 3] : v1[e & 3];
;                         if (kind == 0) x = -0.6065306597126334f * sigmoidf_(x);
;                         else if (kind == 1) x = sigmoidf_(x);
;                         o[e] = x; }
;                     u32x4 w; w.x = cvt_pk_bf16(o[0], o[1]); w.y = cvt_pk_bf16(o[2], o[3]); w.z = cvt_pk_bf16(o[4], o[5]); w.w = cvt_pk_bf16(o[6], o[7]);
;                     *(u32x4*)(O + row * 512 + col) = w; } }
	v_mul_f32_e32 v94, s0, v94
	v_mul_f32_e32 v95, s0, v95
	v_mul_f32_e32 v84, s0, v84
	v_mul_f32_e32 v85, s0, v85
	v_mul_f32_e32 v86, s0, v86
	v_mul_f32_e32 v87, s0, v87
	s_mov_b64 s[98:99], 0x24000
	v_lshl_add_u64 v[158:159], v[156:157], 0, s[98:99]
	v_cvt_pk_bf16_f32 v192, v92, v93
	v_cvt_pk_bf16_f32 v193, v94, v95
	v_cvt_pk_bf16_f32 v194, v84, v85
	v_cvt_pk_bf16_f32 v195, v86, v87
	global_store_dwordx4 v[158:159], v[192:195], off
	v_pk_add_f32 v[76:77], v[76:77], v[164:165]
	v_pk_add_f32 v[78:79], v[78:79], v[166:167]
	v_pk_add_f32 v[72:73], v[72:73], v[168:169]
	v_pk_add_f32 v[74:75], v[74:75], v[170:171]
	v_mul_f32_e32 v76, 0xbfb8aa3b, v76
	v_mul_f32_e32 v77, 0xbfb8aa3b, v77
	v_mul_f32_e32 v78, 0xbfb8aa3b, v78
	v_mul_f32_e32 v79, 0xbfb8aa3b, v79
	v_mul_f32_e32 v72, 0xbfb8aa3b, v72
	v_mul_f32_e32 v73, 0xbfb8aa3b, v73
	v_mul_f32_e32 v74, 0xbfb8aa3b, v74
	v_mul_f32_e32 v75, 0xbfb8aa3b, v75
	v_exp_f32_e32 v76, v76
	v_exp_f32_e32 v77, v77
	v_exp_f32_e32 v78, v78
	v_exp_f32_e32 v79, v79
	v_exp_f32_e32 v72, v72
	v_exp_f32_e32 v73, v73
	v_exp_f32_e32 v74, v74
	v_exp_f32_e32 v75, v75
	v_pk_add_f32 v[76:77], v[76:77], 1.0 op_sel_hi:[1,0]
	v_pk_add_f32 v[78:79], v[78:79], 1.0 op_sel_hi:[1,0]
	v_pk_add_f32 v[72:73], v[72:73], 1.0 op_sel_hi:[1,0]
	v_pk_add_f32 v[74:75], v[74:75], 1.0 op_sel_hi:[1,0]
	v_div_scale_f32 v180, s[100:101], v76, v76, 1.0
	v_rcp_f32_e32 v181, v180
	v_div_scale_f32 v182, vcc, 1.0, v76, 1.0
	v_fma_f32 v183, -v180, v181, 1.0
	v_fmac_f32_e32 v181, v183, v181
	v_mul_f32_e32 v183, v182, v181
	v_fma_f32 v184, -v180, v183, v182
	v_fmac_f32_e32 v183, v184, v181
	v_fma_f32 v180, -v180, v183, v182
	v_div_fmas_f32 v180, v180, v181, v183
	v_div_fixup_f32 v76, v180, v76, 1.0
	v_div_scale_f32 v180, s[100:101], v77, v77, 1.0
	v_rcp_f32_e32 v181, v180
	v_div_scale_f32 v182, vcc, 1.0, v77, 1.0
	v_fma_f32 v183, -v180, v181, 1.0
	v_fmac_f32_e32 v181, v183, v181
	v_mul_f32_e32 v183, v182, v181
	v_fma_f32 v184, -v180, v183, v182
	v_fmac_f32_e32 v183, v184, v181
	v_fma_f32 v180, -v180, v183, v182
	v_div_fmas_f32 v180, v180, v181, v183
	v_div_fixup_f32 v77, v180, v77, 1.0
	v_div_scale_f32 v180, s[100:101], v78, v78, 1.0
	v_rcp_f32_e32 v181, v180
	v_div_scale_f32 v182, vcc, 1.0, v78, 1.0
	v_fma_f32 v183, -v180, v181, 1.0
	v_fmac_f32_e32 v181, v183, v181
	v_mul_f32_e32 v183, v182, v181
	v_fma_f32 v184, -v180, v183, v182
	v_fmac_f32_e32 v183, v184, v181
	v_fma_f32 v180, -v180, v183, v182
	v_div_fmas_f32 v180, v180, v181, v183
	v_div_fixup_f32 v78, v180, v78, 1.0
	v_div_scale_f32 v180, s[100:101], v79, v79, 1.0
	v_rcp_f32_e32 v181, v180
	v_div_scale_f32 v182, vcc, 1.0, v79, 1.0
	v_fma_f32 v183, -v180, v181, 1.0
	v_fmac_f32_e32 v181, v183, v181
	v_mul_f32_e32 v183, v182, v181
	v_fma_f32 v184, -v180, v183, v182
	v_fmac_f32_e32 v183, v184, v181
	v_fma_f32 v180, -v180, v183, v182
	v_div_fmas_f32 v180, v180, v181, v183
	v_div_fixup_f32 v79, v180, v79, 1.0
	v_div_scale_f32 v180, s[100:101], v72, v72, 1.0
	v_rcp_f32_e32 v181, v180
	v_div_scale_f32 v182, vcc, 1.0, v72, 1.0
	v_fma_f32 v183, -v180, v181, 1.0
	v_fmac_f32_e32 v181, v183, v181
	v_mul_f32_e32 v183, v182, v181
	v_fma_f32 v184, -v180, v183, v182
	v_fmac_f32_e32 v183, v184, v181
	v_fma_f32 v180, -v180, v183, v182
	v_div_fmas_f32 v180, v180, v181, v183
	v_div_fixup_f32 v72, v180, v72, 1.0
	v_div_scale_f32 v180, s[100:101], v73, v73, 1.0
	v_rcp_f32_e32 v181, v180
	v_div_scale_f32 v182, vcc, 1.0, v73, 1.0
	v_fma_f32 v183, -v180, v181, 1.0
	v_fmac_f32_e32 v181, v183, v181
	v_mul_f32_e32 v183, v182, v181
	v_fma_f32 v184, -v180, v183, v182
	v_fmac_f32_e32 v183, v184, v181
	v_fma_f32 v180, -v180, v183, v182
	v_div_fmas_f32 v180, v180, v181, v183
	v_div_fixup_f32 v73, v180, v73, 1.0
	v_div_scale_f32 v180, s[100:101], v74, v74, 1.0
	v_rcp_f32_e32 v181, v180
	v_div_scale_f32 v182, vcc, 1.0, v74, 1.0
	v_fma_f32 v183, -v180, v181, 1.0
	v_fmac_f32_e32 v181, v183, v181
	v_mul_f32_e32 v183, v182, v181
	v_fma_f32 v184, -v180, v183, v182
	v_fmac_f32_e32 v183, v184, v181
	v_fma_f32 v180, -v180, v183, v182
	v_div_fmas_f32 v180, v180, v181, v183
	v_div_fixup_f32 v74, v180, v74, 1.0
	v_div_scale_f32 v180, s[100:101], v75, v75, 1.0
	v_rcp_f32_e32 v181, v180
	v_div_scale_f32 v182, vcc, 1.0, v75, 1.0
	v_fma_f32 v183, -v180, v181, 1.0
	v_fmac_f32_e32 v181, v183, v181
	v_mul_f32_e32 v183, v182, v181
	v_fma_f32 v184, -v180, v183, v182
	v_fmac_f32_e32 v183, v184, v181
	v_fma_f32 v180, -v180, v183, v182
	v_div_fmas_f32 v180, v180, v181, v183
	v_div_fixup_f32 v75, v180, v75, 1.0
	v_mul_f32_e32 v76, s0, v76
	v_mul_f32_e32 v77, s0, v77
	v_mul_f32_e32 v78, s0, v78
	v_mul_f32_e32 v79, s0, v79
	v_mul_f32_e32 v72, s0, v72
	v_mul_f32_e32 v73, s0, v73
	v_mul_f32_e32 v74, s0, v74
	v_mul_f32_e32 v75, s0, v75
	s_mov_b64 s[98:99], 0x28000
	v_lshl_add_u64 v[158:159], v[156:157], 0, s[98:99]
	v_cvt_pk_bf16_f32 v188, v76, v77
	v_cvt_pk_bf16_f32 v189, v78, v79
	v_cvt_pk_bf16_f32 v190, v72, v73
	v_cvt_pk_bf16_f32 v191, v74, v75
	global_store_dwordx4 v[158:159], v[188:191], off
	v_pk_add_f32 v[68:69], v[68:69], v[164:165]
	v_pk_add_f32 v[70:71], v[70:71], v[166:167]
	v_pk_add_f32 v[64:65], v[64:65], v[168:169]
	v_pk_add_f32 v[66:67], v[66:67], v[170:171]
	v_mul_f32_e32 v68, 0xbfb8aa3b, v68
	v_mul_f32_e32 v69, 0xbfb8aa3b, v69
	v_mul_f32_e32 v70, 0xbfb8aa3b, v70
	v_mul_f32_e32 v71, 0xbfb8aa3b, v71
	v_mul_f32_e32 v64, 0xbfb8aa3b, v64
	v_mul_f32_e32 v65, 0xbfb8aa3b, v65
	v_mul_f32_e32 v66, 0xbfb8aa3b, v66
	v_mul_f32_e32 v67, 0xbfb8aa3b, v67
	v_exp_f32_e32 v68, v68
	v_exp_f32_e32 v69, v69
	v_exp_f32_e32 v70, v70
	v_exp_f32_e32 v71, v71
	v_exp_f32_e32 v64, v64
	v_exp_f32_e32 v65, v65
	v_exp_f32_e32 v66, v66
	v_exp_f32_e32 v67, v67
; __device__ __forceinline__ unsigned cvt_pk_bf16(float lo, float hi) { const f32x2c v = {lo, hi}; const bf16x2c b = __builtin_convertvector(v, bf16x2c); return __builtin_bit_cast(unsigned, b); }
; __device__ __forceinline__ float sigmoidf_(float x) { return 1.f / (1.f + __expf(-x)); }
;     __device__ __forceinline__ void operator()(const f32x4 (&acc)[2][2][4][2], const Unit& u, int wr, int wc, int fr, int fq) const {
;     ...
; #pragma unroll
;             for (int ai = 0; ai < 2; ++ai)
; #pragma unroll
;                 for (int m = 0; m < 4; ++m) { const size_t row = (size_t)(row0 + ai * HALF + m * 16);
;                     const f32x4 v0 = acc[ai][bj][m][0] + b0, v1 = acc[ai][bj][m][1] + b1; float o[8];
; #pragma unroll
;                     for (int e = 0; e < 8; ++e) { float x = (e < 4) ? v0[e & 3] : v1[e & 3];
;                         if (kind == 0) x = -0.6065306597126334f * sigmoidf_(x);
;                         else if (kind == 1) x = sigmoidf_(x);
;                         o[e] = x; }
;                     u32x4 w; w.x = cvt_pk_bf16(o[0], o[1]); w.y = cvt_pk_bf16(o[2], o[3]); w.z = cvt_pk_bf16(o[4], o[5]); w.w = cvt_pk_bf16(o[6], o[7]);
;                     *(u32x4*)(O + row * 512 + col) = w; } }
	v_pk_add_f32 v[68:69], v[68:69], 1.0 op_sel_hi:[1,0]
	v_pk_add_f32 v[70:71], v[70:71], 1.0 op_sel_hi:[1,0]
	v_pk_add_f32 v[64:65], v[64:65], 1.0 op_sel_hi:[1,0]
	v_pk_add_f32 v[66:67], v[66:67], 1.0 op_sel_hi:[1,0]
	v_div_scale_f32 v180, s[100:101], v68, v68, 1.0
	v_rcp_f32_e32 v181, v180
	v_div_scale_f32 v182, vcc, 1.0, v68, 1.0
	v_fma_f32 v183, -v180, v181, 1.0
	v_fmac_f32_e32 v181, v183, v181
	v_mul_f32_e32 v183, v182, v181
	v_fma_f32 v184, -v180, v183, v182
	v_fmac_f32_e32 v183, v184, v181
	v_fma_f32 v180, -v180, v183, v182
	v_div_fmas_f32 v180, v180, v181, v183
	v_div_fixup_f32 v68, v180, v68, 1.0
	v_div_scale_f32 v180, s[100:101], v69, v69, 1.0
	v_rcp_f32_e32 v181, v180
	v_div_scale_f32 v182, vcc, 1.0, v69, 1.0
	v_fma_f32 v183, -v180, v181, 1.0
	v_fmac_f32_e32 v181, v183, v181
	v_mul_f32_e32 v183, v182, v181
	v_fma_f32 v184, -v180, v183, v182
	v_fmac_f32_e32 v183, v184, v181
	v_fma_f32 v180, -v180, v183, v182
	v_div_fmas_f32 v180, v180, v181, v183
	v_div_fixup_f32 v69, v180, v69, 1.0
	v_div_scale_f32 v180, s[100:101], v70, v70, 1.0
	v_rcp_f32_e32 v181, v180
	v_div_scale_f32 v182, vcc, 1.0, v70, 1.0
	v_fma_f32 v183, -v180, v181, 1.0
	v_fmac_f32_e32 v181, v183, v181
	v_mul_f32_e32 v183, v182, v181
	v_fma_f32 v184, -v180, v183, v182
	v_fmac_f32_e32 v183, v184, v181
	v_fma_f32 v180, -v180, v183, v182
	v_div_fmas_f32 v180, v180, v181, v183
	v_div_fixup_f32 v70, v180, v70, 1.0
	v_div_scale_f32 v180, s[100:101], v71, v71, 1.0
	v_rcp_f32_e32 v181, v180
	v_div_scale_f32 v182, vcc, 1.0, v71, 1.0
	v_fma_f32 v183, -v180, v181, 1.0
	v_fmac_f32_e32 v181, v183, v181
	v_mul_f32_e32 v183, v182, v181
	v_fma_f32 v184, -v180, v183, v182
	v_fmac_f32_e32 v183, v184, v181
	v_fma_f32 v180, -v180, v183, v182
	v_div_fmas_f32 v180, v180, v181, v183
	v_div_fixup_f32 v71, v180, v71, 1.0
	v_div_scale_f32 v180, s[100:101], v64, v64, 1.0
	v_rcp_f32_e32 v181, v180
	v_div_scale_f32 v182, vcc, 1.0, v64, 1.0
	v_fma_f32 v183, -v180, v181, 1.0
	v_fmac_f32_e32 v181, v183, v181
	v_mul_f32_e32 v183, v182, v181
	v_fma_f32 v184, -v180, v183, v182
	v_fmac_f32_e32 v183, v184, v181
	v_fma_f32 v180, -v180, v183, v182
	v_div_fmas_f32 v180, v180, v181, v183
	v_div_fixup_f32 v64, v180, v64, 1.0
	v_div_scale_f32 v180, s[100:101], v65, v65, 1.0
	v_rcp_f32_e32 v181, v180
	v_div_scale_f32 v182, vcc, 1.0, v65, 1.0
	v_fma_f32 v183, -v180, v181, 1.0
	v_fmac_f32_e32 v181, v183, v181
	v_mul_f32_e32 v183, v182, v181
	v_fma_f32 v184, -v180, v183, v182
	v_fmac_f32_e32 v183, v184, v181
	v_fma_f32 v180, -v180, v183, v182
	v_div_fmas_f32 v180, v180, v181, v183
	v_div_fixup_f32 v65, v180, v65, 1.0
	v_div_scale_f32 v180, s[100:101], v66, v66, 1.0
	v_rcp_f32_e32 v181, v180
	v_div_scale_f32 v182, vcc, 1.0, v66, 1.0
	v_fma_f32 v183, -v180, v181, 1.0
	v_fmac_f32_e32 v181, v183, v181
	v_mul_f32_e32 v183, v182, v181
	v_fma_f32 v184, -v180, v183, v182
	v_fmac_f32_e32 v183, v184, v181
	v_fma_f32 v180, -v180, v183, v182
	v_div_fmas_f32 v180, v180, v181, v183
	v_div_fixup_f32 v66, v180, v66, 1.0
	v_div_scale_f32 v180, s[100:101], v67, v67, 1.0
	v_rcp_f32_e32 v181, v180
	v_div_scale_f32 v182, vcc, 1.0, v67, 1.0
	v_fma_f32 v183, -v180, v181, 1.0
	v_fmac_f32_e32 v181, v183, v181
	v_mul_f32_e32 v183, v182, v181
	v_fma_f32 v184, -v180, v183, v182
	v_fmac_f32_e32 v183, v184, v181
	v_fma_f32 v180, -v180, v183, v182
	v_div_fmas_f32 v180, v180, v181, v183
	v_div_fixup_f32 v67, v180, v67, 1.0
	v_mul_f32_e32 v68, s0, v68
	v_mul_f32_e32 v69, s0, v69
	v_mul_f32_e32 v70, s0, v70
	v_mul_f32_e32 v71, s0, v71
	v_mul_f32_e32 v64, s0, v64
	v_mul_f32_e32 v65, s0, v65
	v_mul_f32_e32 v66, s0, v66
	v_mul_f32_e32 v67, s0, v67
	s_mov_b64 s[98:99], 0x2c000
	v_lshl_add_u64 v[158:159], v[156:157], 0, s[98:99]
	v_cvt_pk_bf16_f32 v192, v68, v69
	v_cvt_pk_bf16_f32 v193, v70, v71
	v_cvt_pk_bf16_f32 v194, v64, v65
	v_cvt_pk_bf16_f32 v195, v66, v67
	global_store_dwordx4 v[158:159], v[192:195], off
	v_pk_add_f32 v[60:61], v[60:61], v[172:173]
	v_pk_add_f32 v[62:63], v[62:63], v[174:175]
	v_pk_add_f32 v[56:57], v[56:57], v[176:177]
	v_pk_add_f32 v[58:59], v[58:59], v[178:179]
	v_mul_f32_e32 v60, 0xbfb8aa3b, v60
	v_mul_f32_e32 v61, 0xbfb8aa3b, v61
	v_mul_f32_e32 v62, 0xbfb8aa3b, v62
	v_mul_f32_e32 v63, 0xbfb8aa3b, v63
	v_mul_f32_e32 v56, 0xbfb8aa3b, v56
	v_mul_f32_e32 v57, 0xbfb8aa3b, v57
	v_mul_f32_e32 v58, 0xbfb8aa3b, v58
	v_mul_f32_e32 v59, 0xbfb8aa3b, v59
	v_exp_f32_e32 v60, v60
	v_exp_f32_e32 v61, v61
	v_exp_f32_e32 v62, v62
	v_exp_f32_e32 v63, v63
	v_exp_f32_e32 v56, v56
	v_exp_f32_e32 v57, v57
	v_exp_f32_e32 v58, v58
	v_exp_f32_e32 v59, v59
	v_pk_add_f32 v[60:61], v[60:61], 1.0 op_sel_hi:[1,0]
	v_pk_add_f32 v[62:63], v[62:63], 1.0 op_sel_hi:[1,0]
	v_pk_add_f32 v[56:57], v[56:57], 1.0 op_sel_hi:[1,0]
	v_pk_add_f32 v[58:59], v[58:59], 1.0 op_sel_hi:[1,0]
	v_div_scale_f32 v180, s[100:101], v60, v60, 1.0
	v_rcp_f32_e32 v181, v180
	v_div_scale_f32 v182, vcc, 1.0, v60, 1.0
	v_fma_f32 v183, -v180, v181, 1.0
	v_fmac_f32_e32 v181, v183, v181
	v_mul_f32_e32 v183, v182, v181
	v_fma_f32 v184, -v180, v183, v182
	v_fmac_f32_e32 v183, v184, v181
	v_fma_f32 v180, -v180, v183, v182
	v_div_fmas_f32 v180, v180, v181, v183
	v_div_fixup_f32 v60, v180, v60, 1.0
	v_div_scale_f32 v180, s[100:101], v61, v61, 1.0
	v_rcp_f32_e32 v181, v180
	v_div_scale_f32 v182, vcc, 1.0, v61, 1.0
	v_fma_f32 v183, -v180, v181, 1.0
	v_fmac_f32_e32 v181, v183, v181
	v_mul_f32_e32 v183, v182, v181
	v_fma_f32 v184, -v180, v183, v182
	v_fmac_f32_e32 v183, v184, v181
	v_fma_f32 v180, -v180, v183, v182
	v_div_fmas_f32 v180, v180, v181, v183
	v_div_fixup_f32 v61, v180, v61, 1.0
	v_div_scale_f32 v180, s[100:101], v62, v62, 1.0
	v_rcp_f32_e32 v181, v180
	v_div_scale_f32 v182, vcc, 1.0, v62, 1.0
; __device__ __forceinline__ unsigned cvt_pk_bf16(float lo, float hi) { const f32x2c v = {lo, hi}; const bf16x2c b = __builtin_convertvector(v, bf16x2c); return __builtin_bit_cast(unsigned, b); }
; __device__ __forceinline__ float sigmoidf_(float x) { return 1.f / (1.f + __expf(-x)); }
;     __device__ __forceinline__ void operator()(const f32x4 (&acc)[2][2][4][2], const Unit& u, int wr, int wc, int fr, int fq) const {
;     ...
; #pragma unroll
;             for (int ai = 0; ai < 2; ++ai)
; #pragma unroll
;                 for (int m = 0; m < 4; ++m) { const size_t row = (size_t)(row0 + ai * HALF + m * 16);
;                     const f32x4 v0 = acc[ai][bj][m][0] + b0, v1 = acc[ai][bj][m][1] + b1; float o[8];
; #pragma unroll
;                     for (int e = 0; e < 8; ++e) { float x = (e < 4) ? v0[e & 3] : v1[e & 3];
;                         if (kind == 0) x = -0.6065306597126334f * sigmoidf_(x);
;                         else if (kind == 1) x = sigmoidf_(x);
;                         o[e] = x; }
;                     u32x4 w; w.x = cvt_pk_bf16(o[0], o[1]); w.y = cvt_pk_bf16(o[2], o[3]); w.z = cvt_pk_bf16(o[4], o[5]); w.w = cvt_pk_bf16(o[6], o[7]);
;                     *(u32x4*)(O + row * 512 + col) = w; } }
	v_fma_f32 v183, -v180, v181, 1.0
	v_fmac_f32_e32 v181, v183, v181
	v_mul_f32_e32 v183, v182, v181
	v_fma_f32 v184, -v180, v183, v182
	v_fmac_f32_e32 v183, v184, v181
	v_fma_f32 v180, -v180, v183, v182
	v_div_fmas_f32 v180, v180, v181, v183
	v_div_fixup_f32 v62, v180, v62, 1.0
	v_div_scale_f32 v180, s[100:101], v63, v63, 1.0
	v_rcp_f32_e32 v181, v180
	v_div_scale_f32 v182, vcc, 1.0, v63, 1.0
	v_fma_f32 v183, -v180, v181, 1.0
	v_fmac_f32_e32 v181, v183, v181
	v_mul_f32_e32 v183, v182, v181
	v_fma_f32 v184, -v180, v183, v182
	v_fmac_f32_e32 v183, v184, v181
	v_fma_f32 v180, -v180, v183, v182
	v_div_fmas_f32 v180, v180, v181, v183
	v_div_fixup_f32 v63, v180, v63, 1.0
	v_div_scale_f32 v180, s[100:101], v56, v56, 1.0
	v_rcp_f32_e32 v181, v180
	v_div_scale_f32 v182, vcc, 1.0, v56, 1.0
	v_fma_f32 v183, -v180, v181, 1.0
	v_fmac_f32_e32 v181, v183, v181
	v_mul_f32_e32 v183, v182, v181
	v_fma_f32 v184, -v180, v183, v182
	v_fmac_f32_e32 v183, v184, v181
	v_fma_f32 v180, -v180, v183, v182
	v_div_fmas_f32 v180, v180, v181, v183
	v_div_fixup_f32 v56, v180, v56, 1.0
	v_div_scale_f32 v180, s[100:101], v57, v57, 1.0
	v_rcp_f32_e32 v181, v180
	v_div_scale_f32 v182, vcc, 1.0, v57, 1.0
	v_fma_f32 v183, -v180, v181, 1.0
	v_fmac_f32_e32 v181, v183, v181
	v_mul_f32_e32 v183, v182, v181
	v_fma_f32 v184, -v180, v183, v182
	v_fmac_f32_e32 v183, v184, v181
	v_fma_f32 v180, -v180, v183, v182
	v_div_fmas_f32 v180, v180, v181, v183
	v_div_fixup_f32 v57, v180, v57, 1.0
	v_div_scale_f32 v180, s[100:101], v58, v58, 1.0
	v_rcp_f32_e32 v181, v180
	v_div_scale_f32 v182, vcc, 1.0, v58, 1.0
	v_fma_f32 v183, -v180, v181, 1.0
	v_fmac_f32_e32 v181, v183, v181
	v_mul_f32_e32 v183, v182, v181
	v_fma_f32 v184, -v180, v183, v182
	v_fmac_f32_e32 v183, v184, v181
	v_fma_f32 v180, -v180, v183, v182
	v_div_fmas_f32 v180, v180, v181, v183
	v_div_fixup_f32 v58, v180, v58, 1.0
	v_div_scale_f32 v180, s[100:101], v59, v59, 1.0
	v_rcp_f32_e32 v181, v180
	v_div_scale_f32 v182, vcc, 1.0, v59, 1.0
	v_fma_f32 v183, -v180, v181, 1.0
	v_fmac_f32_e32 v181, v183, v181
	v_mul_f32_e32 v183, v182, v181
	v_fma_f32 v184, -v180, v183, v182
	v_fmac_f32_e32 v183, v184, v181
	v_fma_f32 v180, -v180, v183, v182
	v_div_fmas_f32 v180, v180, v181, v183
	v_div_fixup_f32 v59, v180, v59, 1.0
	v_mul_f32_e32 v60, s0, v60
	v_mul_f32_e32 v61, s0, v61
	v_mul_f32_e32 v62, s0, v62
	v_mul_f32_e32 v63, s0, v63
	v_mul_f32_e32 v56, s0, v56
	v_mul_f32_e32 v57, s0, v57
	v_mul_f32_e32 v58, s0, v58
	v_mul_f32_e32 v59, s0, v59
	v_cvt_pk_bf16_f32 v188, v60, v61
	v_cvt_pk_bf16_f32 v189, v62, v63
	v_cvt_pk_bf16_f32 v190, v56, v57
	v_cvt_pk_bf16_f32 v191, v58, v59
	global_store_dwordx4 v[156:157], v[188:191], off offset:256
	v_pk_add_f32 v[52:53], v[52:53], v[172:173]
	v_pk_add_f32 v[54:55], v[54:55], v[174:175]
	v_pk_add_f32 v[48:49], v[48:49], v[176:177]
	v_pk_add_f32 v[50:51], v[50:51], v[178:179]
	v_mul_f32_e32 v52, 0xbfb8aa3b, v52
	v_mul_f32_e32 v53, 0xbfb8aa3b, v53
	v_mul_f32_e32 v54, 0xbfb8aa3b, v54
	v_mul_f32_e32 v55, 0xbfb8aa3b, v55
	v_mul_f32_e32 v48, 0xbfb8aa3b, v48
	v_mul_f32_e32 v49, 0xbfb8aa3b, v49
	v_mul_f32_e32 v50, 0xbfb8aa3b, v50
	v_mul_f32_e32 v51, 0xbfb8aa3b, v51
	v_exp_f32_e32 v52, v52
	v_exp_f32_e32 v53, v53
	v_exp_f32_e32 v54, v54
	v_exp_f32_e32 v55, v55
	v_exp_f32_e32 v48, v48
	v_exp_f32_e32 v49, v49
	v_exp_f32_e32 v50, v50
	v_exp_f32_e32 v51, v51
	v_pk_add_f32 v[52:53], v[52:53], 1.0 op_sel_hi:[1,0]
	v_pk_add_f32 v[54:55], v[54:55], 1.0 op_sel_hi:[1,0]
	v_pk_add_f32 v[48:49], v[48:49], 1.0 op_sel_hi:[1,0]
	v_pk_add_f32 v[50:51], v[50:51], 1.0 op_sel_hi:[1,0]
	v_div_scale_f32 v180, s[100:101], v52, v52, 1.0
	v_rcp_f32_e32 v181, v180
	v_div_scale_f32 v182, vcc, 1.0, v52, 1.0
	v_fma_f32 v183, -v180, v181, 1.0
	v_fmac_f32_e32 v181, v183, v181
	v_mul_f32_e32 v183, v182, v181
	v_fma_f32 v184, -v180, v183, v182
	v_fmac_f32_e32 v183, v184, v181
	v_fma_f32 v180, -v180, v183, v182
	v_div_fmas_f32 v180, v180, v181, v183
	v_div_fixup_f32 v52, v180, v52, 1.0
	v_div_scale_f32 v180, s[100:101], v53, v53, 1.0
	v_rcp_f32_e32 v181, v180
	v_div_scale_f32 v182, vcc, 1.0, v53, 1.0
	v_fma_f32 v183, -v180, v181, 1.0
	v_fmac_f32_e32 v181, v183, v181
	v_mul_f32_e32 v183, v182, v181
	v_fma_f32 v184, -v180, v183, v182
	v_fmac_f32_e32 v183, v184, v181
	v_fma_f32 v180, -v180, v183, v182
	v_div_fmas_f32 v180, v180, v181, v183
	v_div_fixup_f32 v53, v180, v53, 1.0
	v_div_scale_f32 v180, s[100:101], v54, v54, 1.0
	v_rcp_f32_e32 v181, v180
	v_div_scale_f32 v182, vcc, 1.0, v54, 1.0
	v_fma_f32 v183, -v180, v181, 1.0
	v_fmac_f32_e32 v181, v183, v181
	v_mul_f32_e32 v183, v182, v181
	v_fma_f32 v184, -v180, v183, v182
	v_fmac_f32_e32 v183, v184, v181
	v_fma_f32 v180, -v180, v183, v182
	v_div_fmas_f32 v180, v180, v181, v183
	v_div_fixup_f32 v54, v180, v54, 1.0
	v_div_scale_f32 v180, s[100:101], v55, v55, 1.0
	v_rcp_f32_e32 v181, v180
	v_div_scale_f32 v182, vcc, 1.0, v55, 1.0
	v_fma_f32 v183, -v180, v181, 1.0
	v_fmac_f32_e32 v181, v183, v181
	v_mul_f32_e32 v183, v182, v181
	v_fma_f32 v184, -v180, v183, v182
	v_fmac_f32_e32 v183, v184, v181
	v_fma_f32 v180, -v180, v183, v182
	v_div_fmas_f32 v180, v180, v181, v183
	v_div_fixup_f32 v55, v180, v55, 1.0
	v_div_scale_f32 v180, s[100:101], v48, v48, 1.0
	v_rcp_f32_e32 v181, v180
	v_div_scale_f32 v182, vcc, 1.0, v48, 1.0
	v_fma_f32 v183, -v180, v181, 1.0
	v_fmac_f32_e32 v181, v183, v181
	v_mul_f32_e32 v183, v182, v181
	v_fma_f32 v184, -v180, v183, v182
	v_fmac_f32_e32 v183, v184, v181
	v_fma_f32 v180, -v180, v183, v182
	v_div_fmas_f32 v180, v180, v181, v183
	v_div_fixup_f32 v48, v180, v48, 1.0
	v_div_scale_f32 v180, s[100:101], v49, v49, 1.0
	v_rcp_f32_e32 v181, v180
	v_div_scale_f32 v182, vcc, 1.0, v49, 1.0
; __device__ __forceinline__ unsigned cvt_pk_bf16(float lo, float hi) { const f32x2c v = {lo, hi}; const bf16x2c b = __builtin_convertvector(v, bf16x2c); return __builtin_bit_cast(unsigned, b); }
; __device__ __forceinline__ float sigmoidf_(float x) { return 1.f / (1.f + __expf(-x)); }
;     __device__ __forceinline__ void operator()(const f32x4 (&acc)[2][2][4][2], const Unit& u, int wr, int wc, int fr, int fq) const {
;     ...
; #pragma unroll
;             for (int ai = 0; ai < 2; ++ai)
; #pragma unroll
;                 for (int m = 0; m < 4; ++m) { const size_t row = (size_t)(row0 + ai * HALF + m * 16);
;                     const f32x4 v0 = acc[ai][bj][m][0] + b0, v1 = acc[ai][bj][m][1] + b1; float o[8];
; #pragma unroll
;                     for (int e = 0; e < 8; ++e) { float x = (e < 4) ? v0[e & 3] : v1[e & 3];
;                         if (kind == 0) x = -0.6065306597126334f * sigmoidf_(x);
;                         else if (kind == 1) x = sigmoidf_(x);
;                         o[e] = x; }
;                     u32x4 w; w.x = cvt_pk_bf16(o[0], o[1]); w.y = cvt_pk_bf16(o[2], o[3]); w.z = cvt_pk_bf16(o[4], o[5]); w.w = cvt_pk_bf16(o[6], o[7]);
;                     *(u32x4*)(O + row * 512 + col) = w; } }
	v_fma_f32 v183, -v180, v181, 1.0
	v_fmac_f32_e32 v181, v183, v181
	v_mul_f32_e32 v183, v182, v181
	v_fma_f32 v184, -v180, v183, v182
	v_fmac_f32_e32 v183, v184, v181
	v_fma_f32 v180, -v180, v183, v182
	v_div_fmas_f32 v180, v180, v181, v183
	v_div_fixup_f32 v49, v180, v49, 1.0
	v_div_scale_f32 v180, s[100:101], v50, v50, 1.0
	v_rcp_f32_e32 v181, v180
	v_div_scale_f32 v182, vcc, 1.0, v50, 1.0
	v_fma_f32 v183, -v180, v181, 1.0
	v_fmac_f32_e32 v181, v183, v181
	v_mul_f32_e32 v183, v182, v181
	v_fma_f32 v184, -v180, v183, v182
	v_fmac_f32_e32 v183, v184, v181
	v_fma_f32 v180, -v180, v183, v182
	v_div_fmas_f32 v180, v180, v181, v183
	v_div_fixup_f32 v50, v180, v50, 1.0
	v_div_scale_f32 v180, s[100:101], v51, v51, 1.0
	v_rcp_f32_e32 v181, v180
	v_div_scale_f32 v182, vcc, 1.0, v51, 1.0
	v_fma_f32 v183, -v180, v181, 1.0
	v_fmac_f32_e32 v181, v183, v181
	v_mul_f32_e32 v183, v182, v181
	v_fma_f32 v184, -v180, v183, v182
	v_fmac_f32_e32 v183, v184, v181
	v_fma_f32 v180, -v180, v183, v182
	v_div_fmas_f32 v180, v180, v181, v183
	v_div_fixup_f32 v51, v180, v51, 1.0
	v_mul_f32_e32 v52, s0, v52
	v_mul_f32_e32 v53, s0, v53
	v_mul_f32_e32 v54, s0, v54
	v_mul_f32_e32 v55, s0, v55
	v_mul_f32_e32 v48, s0, v48
	v_mul_f32_e32 v49, s0, v49
	v_mul_f32_e32 v50, s0, v50
	v_mul_f32_e32 v51, s0, v51
	s_mov_b64 s[98:99], 0x4000
	v_lshl_add_u64 v[158:159], v[156:157], 0, s[98:99]
	v_cvt_pk_bf16_f32 v192, v52, v53
	v_cvt_pk_bf16_f32 v193, v54, v55
	v_cvt_pk_bf16_f32 v194, v48, v49
	v_cvt_pk_bf16_f32 v195, v50, v51
	global_store_dwordx4 v[158:159], v[192:195], off offset:256
	v_pk_add_f32 v[44:45], v[44:45], v[172:173]
	v_pk_add_f32 v[46:47], v[46:47], v[174:175]
	v_pk_add_f32 v[40:41], v[40:41], v[176:177]
	v_pk_add_f32 v[42:43], v[42:43], v[178:179]
	v_mul_f32_e32 v44, 0xbfb8aa3b, v44
	v_mul_f32_e32 v45, 0xbfb8aa3b, v45
	v_mul_f32_e32 v46, 0xbfb8aa3b, v46
	v_mul_f32_e32 v47, 0xbfb8aa3b, v47
	v_mul_f32_e32 v40, 0xbfb8aa3b, v40
	v_mul_f32_e32 v41, 0xbfb8aa3b, v41
	v_mul_f32_e32 v42, 0xbfb8aa3b, v42
	v_mul_f32_e32 v43, 0xbfb8aa3b, v43
	v_exp_f32_e32 v44, v44
	v_exp_f32_e32 v45, v45
	v_exp_f32_e32 v46, v46
	v_exp_f32_e32 v47, v47
	v_exp_f32_e32 v40, v40
	v_exp_f32_e32 v41, v41
	v_exp_f32_e32 v42, v42
	v_exp_f32_e32 v43, v43
	v_pk_add_f32 v[44:45], v[44:45], 1.0 op_sel_hi:[1,0]
	v_pk_add_f32 v[46:47], v[46:47], 1.0 op_sel_hi:[1,0]
	v_pk_add_f32 v[40:41], v[40:41], 1.0 op_sel_hi:[1,0]
	v_pk_add_f32 v[42:43], v[42:43], 1.0 op_sel_hi:[1,0]
	v_div_scale_f32 v180, s[100:101], v44, v44, 1.0
	v_rcp_f32_e32 v181, v180
	v_div_scale_f32 v182, vcc, 1.0, v44, 1.0
	v_fma_f32 v183, -v180, v181, 1.0
	v_fmac_f32_e32 v181, v183, v181
	v_mul_f32_e32 v183, v182, v181
	v_fma_f32 v184, -v180, v183, v182
	v_fmac_f32_e32 v183, v184, v181
	v_fma_f32 v180, -v180, v183, v182
	v_div_fmas_f32 v180, v180, v181, v183
	v_div_fixup_f32 v44, v180, v44, 1.0
	v_div_scale_f32 v180, s[100:101], v45, v45, 1.0
	v_rcp_f32_e32 v181, v180
	v_div_scale_f32 v182, vcc, 1.0, v45, 1.0
	v_fma_f32 v183, -v180, v181, 1.0
	v_fmac_f32_e32 v181, v183, v181
	v_mul_f32_e32 v183, v182, v181
	v_fma_f32 v184, -v180, v183, v182
	v_fmac_f32_e32 v183, v184, v181
	v_fma_f32 v180, -v180, v183, v182
	v_div_fmas_f32 v180, v180, v181, v183
	v_div_fixup_f32 v45, v180, v45, 1.0
	v_div_scale_f32 v180, s[100:101], v46, v46, 1.0
	v_rcp_f32_e32 v181, v180
	v_div_scale_f32 v182, vcc, 1.0, v46, 1.0
	v_fma_f32 v183, -v180, v181, 1.0
	v_fmac_f32_e32 v181, v183, v181
	v_mul_f32_e32 v183, v182, v181
	v_fma_f32 v184, -v180, v183, v182
	v_fmac_f32_e32 v183, v184, v181
	v_fma_f32 v180, -v180, v183, v182
	v_div_fmas_f32 v180, v180, v181, v183
	v_div_fixup_f32 v46, v180, v46, 1.0
	v_div_scale_f32 v180, s[100:101], v47, v47, 1.0
	v_rcp_f32_e32 v181, v180
	v_div_scale_f32 v182, vcc, 1.0, v47, 1.0
	v_fma_f32 v183, -v180, v181, 1.0
	v_fmac_f32_e32 v181, v183, v181
	v_mul_f32_e32 v183, v182, v181
	v_fma_f32 v184, -v180, v183, v182
	v_fmac_f32_e32 v183, v184, v181
	v_fma_f32 v180, -v180, v183, v182
	v_div_fmas_f32 v180, v180, v181, v183
	v_div_fixup_f32 v47, v180, v47, 1.0
	v_div_scale_f32 v180, s[100:101], v40, v40, 1.0
	v_rcp_f32_e32 v181, v180
	v_div_scale_f32 v182, vcc, 1.0, v40, 1.0
	v_fma_f32 v183, -v180, v181, 1.0
	v_fmac_f32_e32 v181, v183, v181
	v_mul_f32_e32 v183, v182, v181
	v_fma_f32 v184, -v180, v183, v182
	v_fmac_f32_e32 v183, v184, v181
	v_fma_f32 v180, -v180, v183, v182
	v_div_fmas_f32 v180, v180, v181, v183
	v_div_fixup_f32 v40, v180, v40, 1.0
	v_div_scale_f32 v180, s[100:101], v41, v41, 1.0
	v_rcp_f32_e32 v181, v180
	v_div_scale_f32 v182, vcc, 1.0, v41, 1.0
	v_fma_f32 v183, -v180, v181, 1.0
	v_fmac_f32_e32 v181, v183, v181
	v_mul_f32_e32 v183, v182, v181
	v_fma_f32 v184, -v180, v183, v182
	v_fmac_f32_e32 v183, v184, v181
	v_fma_f32 v180, -v180, v183, v182
	v_div_fmas_f32 v180, v180, v181, v183
	v_div_fixup_f32 v41, v180, v41, 1.0
	v_div_scale_f32 v180, s[100:101], v42, v42, 1.0
	v_rcp_f32_e32 v181, v180
	v_div_scale_f32 v182, vcc, 1.0, v42, 1.0
	v_fma_f32 v183, -v180, v181, 1.0
	v_fmac_f32_e32 v181, v183, v181
	v_mul_f32_e32 v183, v182, v181
	v_fma_f32 v184, -v180, v183, v182
	v_fmac_f32_e32 v183, v184, v181
	v_fma_f32 v180, -v180, v183, v182
	v_div_fmas_f32 v180, v180, v181, v183
	v_div_fixup_f32 v42, v180, v42, 1.0
	v_div_scale_f32 v180, s[100:101], v43, v43, 1.0
	v_rcp_f32_e32 v181, v180
	v_div_scale_f32 v182, vcc, 1.0, v43, 1.0
	v_fma_f32 v183, -v180, v181, 1.0
	v_fmac_f32_e32 v181, v183, v181
	v_mul_f32_e32 v183, v182, v181
	v_fma_f32 v184, -v180, v183, v182
	v_fmac_f32_e32 v183, v184, v181
	v_fma_f32 v180, -v180, v183, v182
	v_div_fmas_f32 v180, v180, v181, v183
	v_div_fixup_f32 v43, v180, v43, 1.0
	v_mul_f32_e32 v44, s0, v44
; __device__ __forceinline__ float sigmoidf_(float x) { return 1.f / (1.f + __expf(-x)); }
; __device__ __forceinline__ unsigned cvt_pk_bf16(float lo, float hi) { const f32x2c v = {lo, hi}; const bf16x2c b = __builtin_convertvector(v, bf16x2c); return __builtin_bit_cast(unsigned, b); }
;     __device__ __forceinline__ void operator()(const f32x4 (&acc)[2][2][4][2], const Unit& u, int wr, int wc, int fr, int fq) const {
;     ...
;                 for (int m = 0; m < 4; ++m) { const size_t row = (size_t)(row0 + ai * HALF + m * 16);
;                     const f32x4 v0 = acc[ai][bj][m][0] + b0, v1 = acc[ai][bj][m][1] + b1; float o[8];
; #pragma unroll
;                     for (int e = 0; e < 8; ++e) { float x = (e < 4) ? v0[e & 3] : v1[e & 3];
;                         if (kind == 0) x = -0.6065306597126334f * sigmoidf_(x);
;                         else if (kind == 1) x = sigmoidf_(x);
;                         o[e] = x; }
;                     u32x4 w; w.x = cvt_pk_bf16(o[0], o[1]); w.y = cvt_pk_bf16(o[2], o[3]); w.z = cvt_pk_bf16(o[4], o[5]); w.w = cvt_pk_bf16(o[6], o[7]);
;                     *(u32x4*)(O + row * 512 + col) = w; } }
	v_mul_f32_e32 v45, s0, v45
	v_mul_f32_e32 v46, s0, v46
	v_mul_f32_e32 v47, s0, v47
	v_mul_f32_e32 v40, s0, v40
	v_mul_f32_e32 v41, s0, v41
	v_mul_f32_e32 v42, s0, v42
	v_mul_f32_e32 v43, s0, v43
	s_mov_b64 s[98:99], 0x8000
	v_lshl_add_u64 v[158:159], v[156:157], 0, s[98:99]
	v_cvt_pk_bf16_f32 v188, v44, v45
	v_cvt_pk_bf16_f32 v189, v46, v47
	v_cvt_pk_bf16_f32 v190, v40, v41
	v_cvt_pk_bf16_f32 v191, v42, v43
	global_store_dwordx4 v[158:159], v[188:191], off offset:256
	v_pk_add_f32 v[36:37], v[36:37], v[172:173]
	v_pk_add_f32 v[38:39], v[38:39], v[174:175]
	v_pk_add_f32 v[32:33], v[32:33], v[176:177]
	v_pk_add_f32 v[34:35], v[34:35], v[178:179]
	v_mul_f32_e32 v36, 0xbfb8aa3b, v36
	v_mul_f32_e32 v37, 0xbfb8aa3b, v37
	v_mul_f32_e32 v38, 0xbfb8aa3b, v38
	v_mul_f32_e32 v39, 0xbfb8aa3b, v39
	v_mul_f32_e32 v32, 0xbfb8aa3b, v32
	v_mul_f32_e32 v33, 0xbfb8aa3b, v33
	v_mul_f32_e32 v34, 0xbfb8aa3b, v34
	v_mul_f32_e32 v35, 0xbfb8aa3b, v35
	v_exp_f32_e32 v36, v36
	v_exp_f32_e32 v37, v37
	v_exp_f32_e32 v38, v38
	v_exp_f32_e32 v39, v39
	v_exp_f32_e32 v32, v32
	v_exp_f32_e32 v33, v33
	v_exp_f32_e32 v34, v34
	v_exp_f32_e32 v35, v35
	v_pk_add_f32 v[36:37], v[36:37], 1.0 op_sel_hi:[1,0]
	v_pk_add_f32 v[38:39], v[38:39], 1.0 op_sel_hi:[1,0]
	v_pk_add_f32 v[32:33], v[32:33], 1.0 op_sel_hi:[1,0]
	v_pk_add_f32 v[34:35], v[34:35], 1.0 op_sel_hi:[1,0]
	v_div_scale_f32 v180, s[100:101], v36, v36, 1.0
	v_rcp_f32_e32 v181, v180
	v_div_scale_f32 v182, vcc, 1.0, v36, 1.0
	v_fma_f32 v183, -v180, v181, 1.0
	v_fmac_f32_e32 v181, v183, v181
	v_mul_f32_e32 v183, v182, v181
	v_fma_f32 v184, -v180, v183, v182
	v_fmac_f32_e32 v183, v184, v181
	v_fma_f32 v180, -v180, v183, v182
	v_div_fmas_f32 v180, v180, v181, v183
	v_div_fixup_f32 v36, v180, v36, 1.0
	v_div_scale_f32 v180, s[100:101], v37, v37, 1.0
	v_rcp_f32_e32 v181, v180
	v_div_scale_f32 v182, vcc, 1.0, v37, 1.0
	v_fma_f32 v183, -v180, v181, 1.0
	v_fmac_f32_e32 v181, v183, v181
	v_mul_f32_e32 v183, v182, v181
	v_fma_f32 v184, -v180, v183, v182
	v_fmac_f32_e32 v183, v184, v181
	v_fma_f32 v180, -v180, v183, v182
	v_div_fmas_f32 v180, v180, v181, v183
	v_div_fixup_f32 v37, v180, v37, 1.0
	v_div_scale_f32 v180, s[100:101], v38, v38, 1.0
	v_rcp_f32_e32 v181, v180
	v_div_scale_f32 v182, vcc, 1.0, v38, 1.0
	v_fma_f32 v183, -v180, v181, 1.0
	v_fmac_f32_e32 v181, v183, v181
	v_mul_f32_e32 v183, v182, v181
	v_fma_f32 v184, -v180, v183, v182
	v_fmac_f32_e32 v183, v184, v181
	v_fma_f32 v180, -v180, v183, v182
	v_div_fmas_f32 v180, v180, v181, v183
	v_div_fixup_f32 v38, v180, v38, 1.0
	v_div_scale_f32 v180, s[100:101], v39, v39, 1.0
	v_rcp_f32_e32 v181, v180
	v_div_scale_f32 v182, vcc, 1.0, v39, 1.0
	v_fma_f32 v183, -v180, v181, 1.0
	v_fmac_f32_e32 v181, v183, v181
	v_mul_f32_e32 v183, v182, v181
	v_fma_f32 v184, -v180, v183, v182
	v_fmac_f32_e32 v183, v184, v181
	v_fma_f32 v180, -v180, v183, v182
	v_div_fmas_f32 v180, v180, v181, v183
	v_div_fixup_f32 v39, v180, v39, 1.0
	v_div_scale_f32 v180, s[100:101], v32, v32, 1.0
	v_rcp_f32_e32 v181, v180
	v_div_scale_f32 v182, vcc, 1.0, v32, 1.0
	v_fma_f32 v183, -v180, v181, 1.0
	v_fmac_f32_e32 v181, v183, v181
	v_mul_f32_e32 v183, v182, v181
	v_fma_f32 v184, -v180, v183, v182
	v_fmac_f32_e32 v183, v184, v181
	v_fma_f32 v180, -v180, v183, v182
	v_div_fmas_f32 v180, v180, v181, v183
	v_div_fixup_f32 v32, v180, v32, 1.0
	v_div_scale_f32 v180, s[100:101], v33, v33, 1.0
	v_rcp_f32_e32 v181, v180
	v_div_scale_f32 v182, vcc, 1.0, v33, 1.0
	v_fma_f32 v183, -v180, v181, 1.0
	v_fmac_f32_e32 v181, v183, v181
	v_mul_f32_e32 v183, v182, v181
	v_fma_f32 v184, -v180, v183, v182
	v_fmac_f32_e32 v183, v184, v181
	v_fma_f32 v180, -v180, v183, v182
	v_div_fmas_f32 v180, v180, v181, v183
	v_div_fixup_f32 v33, v180, v33, 1.0
	v_div_scale_f32 v180, s[100:101], v34, v34, 1.0
	v_rcp_f32_e32 v181, v180
	v_div_scale_f32 v182, vcc, 1.0, v34, 1.0
	v_fma_f32 v183, -v180, v181, 1.0
	v_fmac_f32_e32 v181, v183, v181
	v_mul_f32_e32 v183, v182, v181
	v_fma_f32 v184, -v180, v183, v182
	v_fmac_f32_e32 v183, v184, v181
	v_fma_f32 v180, -v180, v183, v182
	v_div_fmas_f32 v180, v180, v181, v183
	v_div_fixup_f32 v34, v180, v34, 1.0
	v_div_scale_f32 v180, s[100:101], v35, v35, 1.0
	v_rcp_f32_e32 v181, v180
	v_div_scale_f32 v182, vcc, 1.0, v35, 1.0
	v_fma_f32 v183, -v180, v181, 1.0
	v_fmac_f32_e32 v181, v183, v181
	v_mul_f32_e32 v183, v182, v181
	v_fma_f32 v184, -v180, v183, v182
	v_fmac_f32_e32 v183, v184, v181
	v_fma_f32 v180, -v180, v183, v182
	v_div_fmas_f32 v180, v180, v181, v183
	v_div_fixup_f32 v35, v180, v35, 1.0
	v_mul_f32_e32 v36, s0, v36
	v_mul_f32_e32 v37, s0, v37
	v_mul_f32_e32 v38, s0, v38
	v_mul_f32_e32 v39, s0, v39
	v_mul_f32_e32 v32, s0, v32
	v_mul_f32_e32 v33, s0, v33
	v_mul_f32_e32 v34, s0, v34
	v_mul_f32_e32 v35, s0, v35
	s_mov_b64 s[98:99], 0xc000
	v_lshl_add_u64 v[158:159], v[156:157], 0, s[98:99]
	v_cvt_pk_bf16_f32 v192, v36, v37
	v_cvt_pk_bf16_f32 v193, v38, v39
	v_cvt_pk_bf16_f32 v194, v32, v33
	v_cvt_pk_bf16_f32 v195, v34, v35
	global_store_dwordx4 v[158:159], v[192:195], off offset:256
	v_pk_add_f32 v[28:29], v[28:29], v[172:173]
	v_pk_add_f32 v[30:31], v[30:31], v[174:175]
	v_pk_add_f32 v[24:25], v[24:25], v[176:177]
	v_pk_add_f32 v[26:27], v[26:27], v[178:179]
	v_mul_f32_e32 v28, 0xbfb8aa3b, v28
	v_mul_f32_e32 v29, 0xbfb8aa3b, v29
	v_mul_f32_e32 v30, 0xbfb8aa3b, v30
	v_mul_f32_e32 v31, 0xbfb8aa3b, v31
	v_mul_f32_e32 v24, 0xbfb8aa3b, v24
	v_mul_f32_e32 v25, 0xbfb8aa3b, v25
	v_mul_f32_e32 v26, 0xbfb8aa3b, v26
	v_mul_f32_e32 v27, 0xbfb8aa3b, v27
	v_exp_f32_e32 v28, v28
	v_exp_f32_e32 v29, v29
	v_exp_f32_e32 v30, v30
	v_exp_f32_e32 v31, v31
	v_exp_f32_e32 v24, v24
	v_exp_f32_e32 v25, v25
	v_exp_f32_e32 v26, v26
; __device__ __forceinline__ float sigmoidf_(float x) { return 1.f / (1.f + __expf(-x)); }
; __device__ __forceinline__ unsigned cvt_pk_bf16(float lo, float hi) { const f32x2c v = {lo, hi}; const bf16x2c b = __builtin_convertvector(v, bf16x2c); return __builtin_bit_cast(unsigned, b); }
;     __device__ __forceinline__ void operator()(const f32x4 (&acc)[2][2][4][2], const Unit& u, int wr, int wc, int fr, int fq) const {
;     ...
;                 for (int m = 0; m < 4; ++m) { const size_t row = (size_t)(row0 + ai * HALF + m * 16);
;                     const f32x4 v0 = acc[ai][bj][m][0] + b0, v1 = acc[ai][bj][m][1] + b1; float o[8];
; #pragma unroll
;                     for (int e = 0; e < 8; ++e) { float x = (e < 4) ? v0[e & 3] : v1[e & 3];
;                         if (kind == 0) x = -0.6065306597126334f * sigmoidf_(x);
;                         else if (kind == 1) x = sigmoidf_(x);
;                         o[e] = x; }
;                     u32x4 w; w.x = cvt_pk_bf16(o[0], o[1]); w.y = cvt_pk_bf16(o[2], o[3]); w.z = cvt_pk_bf16(o[4], o[5]); w.w = cvt_pk_bf16(o[6], o[7]);
;                     *(u32x4*)(O + row * 512 + col) = w; } }
	v_exp_f32_e32 v27, v27
	v_pk_add_f32 v[28:29], v[28:29], 1.0 op_sel_hi:[1,0]
	v_pk_add_f32 v[30:31], v[30:31], 1.0 op_sel_hi:[1,0]
	v_pk_add_f32 v[24:25], v[24:25], 1.0 op_sel_hi:[1,0]
	v_pk_add_f32 v[26:27], v[26:27], 1.0 op_sel_hi:[1,0]
	v_div_scale_f32 v180, s[100:101], v28, v28, 1.0
	v_rcp_f32_e32 v181, v180
	v_div_scale_f32 v182, vcc, 1.0, v28, 1.0
	v_fma_f32 v183, -v180, v181, 1.0
	v_fmac_f32_e32 v181, v183, v181
	v_mul_f32_e32 v183, v182, v181
	v_fma_f32 v184, -v180, v183, v182
	v_fmac_f32_e32 v183, v184, v181
	v_fma_f32 v180, -v180, v183, v182
	v_div_fmas_f32 v180, v180, v181, v183
	v_div_fixup_f32 v28, v180, v28, 1.0
	v_div_scale_f32 v180, s[100:101], v29, v29, 1.0
	v_rcp_f32_e32 v181, v180
	v_div_scale_f32 v182, vcc, 1.0, v29, 1.0
	v_fma_f32 v183, -v180, v181, 1.0
	v_fmac_f32_e32 v181, v183, v181
	v_mul_f32_e32 v183, v182, v181
	v_fma_f32 v184, -v180, v183, v182
	v_fmac_f32_e32 v183, v184, v181
	v_fma_f32 v180, -v180, v183, v182
	v_div_fmas_f32 v180, v180, v181, v183
	v_div_fixup_f32 v29, v180, v29, 1.0
	v_div_scale_f32 v180, s[100:101], v30, v30, 1.0
	v_rcp_f32_e32 v181, v180
	v_div_scale_f32 v182, vcc, 1.0, v30, 1.0
	v_fma_f32 v183, -v180, v181, 1.0
	v_fmac_f32_e32 v181, v183, v181
	v_mul_f32_e32 v183, v182, v181
	v_fma_f32 v184, -v180, v183, v182
	v_fmac_f32_e32 v183, v184, v181
	v_fma_f32 v180, -v180, v183, v182
	v_div_fmas_f32 v180, v180, v181, v183
	v_div_fixup_f32 v30, v180, v30, 1.0
	v_div_scale_f32 v180, s[100:101], v31, v31, 1.0
	v_rcp_f32_e32 v181, v180
	v_div_scale_f32 v182, vcc, 1.0, v31, 1.0
	v_fma_f32 v183, -v180, v181, 1.0
	v_fmac_f32_e32 v181, v183, v181
	v_mul_f32_e32 v183, v182, v181
	v_fma_f32 v184, -v180, v183, v182
	v_fmac_f32_e32 v183, v184, v181
	v_fma_f32 v180, -v180, v183, v182
	v_div_fmas_f32 v180, v180, v181, v183
	v_div_fixup_f32 v31, v180, v31, 1.0
	v_div_scale_f32 v180, s[100:101], v24, v24, 1.0
	v_rcp_f32_e32 v181, v180
	v_div_scale_f32 v182, vcc, 1.0, v24, 1.0
	v_fma_f32 v183, -v180, v181, 1.0
	v_fmac_f32_e32 v181, v183, v181
	v_mul_f32_e32 v183, v182, v181
	v_fma_f32 v184, -v180, v183, v182
	v_fmac_f32_e32 v183, v184, v181
	v_fma_f32 v180, -v180, v183, v182
	v_div_fmas_f32 v180, v180, v181, v183
	v_div_fixup_f32 v24, v180, v24, 1.0
	v_div_scale_f32 v180, s[100:101], v25, v25, 1.0
	v_rcp_f32_e32 v181, v180
	v_div_scale_f32 v182, vcc, 1.0, v25, 1.0
	v_fma_f32 v183, -v180, v181, 1.0
	v_fmac_f32_e32 v181, v183, v181
	v_mul_f32_e32 v183, v182, v181
	v_fma_f32 v184, -v180, v183, v182
	v_fmac_f32_e32 v183, v184, v181
	v_fma_f32 v180, -v180, v183, v182
	v_div_fmas_f32 v180, v180, v181, v183
	v_div_fixup_f32 v25, v180, v25, 1.0
	v_div_scale_f32 v180, s[100:101], v26, v26, 1.0
	v_rcp_f32_e32 v181, v180
	v_div_scale_f32 v182, vcc, 1.0, v26, 1.0
	v_fma_f32 v183, -v180, v181, 1.0
	v_fmac_f32_e32 v181, v183, v181
	v_mul_f32_e32 v183, v182, v181
	v_fma_f32 v184, -v180, v183, v182
	v_fmac_f32_e32 v183, v184, v181
	v_fma_f32 v180, -v180, v183, v182
	v_div_fmas_f32 v180, v180, v181, v183
	v_div_fixup_f32 v26, v180, v26, 1.0
	v_div_scale_f32 v180, s[100:101], v27, v27, 1.0
	v_rcp_f32_e32 v181, v180
	v_div_scale_f32 v182, vcc, 1.0, v27, 1.0
	v_fma_f32 v183, -v180, v181, 1.0
	v_fmac_f32_e32 v181, v183, v181
	v_mul_f32_e32 v183, v182, v181
	v_fma_f32 v184, -v180, v183, v182
	v_fmac_f32_e32 v183, v184, v181
	v_fma_f32 v180, -v180, v183, v182
	v_div_fmas_f32 v180, v180, v181, v183
	v_div_fixup_f32 v27, v180, v27, 1.0
	v_mul_f32_e32 v28, s0, v28
	v_mul_f32_e32 v29, s0, v29
	v_mul_f32_e32 v30, s0, v30
	v_mul_f32_e32 v31, s0, v31
	v_mul_f32_e32 v24, s0, v24
	v_mul_f32_e32 v25, s0, v25
	v_mul_f32_e32 v26, s0, v26
	v_mul_f32_e32 v27, s0, v27
	s_mov_b64 s[98:99], 0x20000
	v_lshl_add_u64 v[158:159], v[156:157], 0, s[98:99]
	v_cvt_pk_bf16_f32 v188, v28, v29
	v_cvt_pk_bf16_f32 v189, v30, v31
	v_cvt_pk_bf16_f32 v190, v24, v25
	v_cvt_pk_bf16_f32 v191, v26, v27
	global_store_dwordx4 v[158:159], v[188:191], off offset:256
	v_pk_add_f32 v[20:21], v[20:21], v[172:173]
	v_pk_add_f32 v[22:23], v[22:23], v[174:175]
	v_pk_add_f32 v[16:17], v[16:17], v[176:177]
	v_pk_add_f32 v[18:19], v[18:19], v[178:179]
	v_mul_f32_e32 v20, 0xbfb8aa3b, v20
	v_mul_f32_e32 v21, 0xbfb8aa3b, v21
	v_mul_f32_e32 v22, 0xbfb8aa3b, v22
	v_mul_f32_e32 v23, 0xbfb8aa3b, v23
	v_mul_f32_e32 v16, 0xbfb8aa3b, v16
	v_mul_f32_e32 v17, 0xbfb8aa3b, v17
	v_mul_f32_e32 v18, 0xbfb8aa3b, v18
	v_mul_f32_e32 v19, 0xbfb8aa3b, v19
	v_exp_f32_e32 v20, v20
	v_exp_f32_e32 v21, v21
	v_exp_f32_e32 v22, v22
	v_exp_f32_e32 v23, v23
	v_exp_f32_e32 v16, v16
	v_exp_f32_e32 v17, v17
	v_exp_f32_e32 v18, v18
	v_exp_f32_e32 v19, v19
	v_pk_add_f32 v[20:21], v[20:21], 1.0 op_sel_hi:[1,0]
	v_pk_add_f32 v[22:23], v[22:23], 1.0 op_sel_hi:[1,0]
	v_pk_add_f32 v[16:17], v[16:17], 1.0 op_sel_hi:[1,0]
	v_pk_add_f32 v[18:19], v[18:19], 1.0 op_sel_hi:[1,0]
	v_div_scale_f32 v180, s[100:101], v20, v20, 1.0
	v_rcp_f32_e32 v181, v180
	v_div_scale_f32 v182, vcc, 1.0, v20, 1.0
	v_fma_f32 v183, -v180, v181, 1.0
	v_fmac_f32_e32 v181, v183, v181
	v_mul_f32_e32 v183, v182, v181
	v_fma_f32 v184, -v180, v183, v182
	v_fmac_f32_e32 v183, v184, v181
	v_fma_f32 v180, -v180, v183, v182
	v_div_fmas_f32 v180, v180, v181, v183
	v_div_fixup_f32 v20, v180, v20, 1.0
	v_div_scale_f32 v180, s[100:101], v21, v21, 1.0
	v_rcp_f32_e32 v181, v180
	v_div_scale_f32 v182, vcc, 1.0, v21, 1.0
	v_fma_f32 v183, -v180, v181, 1.0
	v_fmac_f32_e32 v181, v183, v181
	v_mul_f32_e32 v183, v182, v181
	v_fma_f32 v184, -v180, v183, v182
	v_fmac_f32_e32 v183, v184, v181
	v_fma_f32 v180, -v180, v183, v182
	v_div_fmas_f32 v180, v180, v181, v183
	v_div_fixup_f32 v21, v180, v21, 1.0
	v_div_scale_f32 v180, s[100:101], v22, v22, 1.0
	v_rcp_f32_e32 v181, v180
; __device__ __forceinline__ float sigmoidf_(float x) { return 1.f / (1.f + __expf(-x)); }
; __device__ __forceinline__ unsigned cvt_pk_bf16(float lo, float hi) { const f32x2c v = {lo, hi}; const bf16x2c b = __builtin_convertvector(v, bf16x2c); return __builtin_bit_cast(unsigned, b); }
;     __device__ __forceinline__ void operator()(const f32x4 (&acc)[2][2][4][2], const Unit& u, int wr, int wc, int fr, int fq) const {
;     ...
;                 for (int m = 0; m < 4; ++m) { const size_t row = (size_t)(row0 + ai * HALF + m * 16);
;                     const f32x4 v0 = acc[ai][bj][m][0] + b0, v1 = acc[ai][bj][m][1] + b1; float o[8];
; #pragma unroll
;                     for (int e = 0; e < 8; ++e) { float x = (e < 4) ? v0[e & 3] : v1[e & 3];
;                         if (kind == 0) x = -0.6065306597126334f * sigmoidf_(x);
;                         else if (kind == 1) x = sigmoidf_(x);
;                         o[e] = x; }
;                     u32x4 w; w.x = cvt_pk_bf16(o[0], o[1]); w.y = cvt_pk_bf16(o[2], o[3]); w.z = cvt_pk_bf16(o[4], o[5]); w.w = cvt_pk_bf16(o[6], o[7]);
;                     *(u32x4*)(O + row * 512 + col) = w; } }
	v_div_scale_f32 v182, vcc, 1.0, v22, 1.0
	v_fma_f32 v183, -v180, v181, 1.0
	v_fmac_f32_e32 v181, v183, v181
	v_mul_f32_e32 v183, v182, v181
	v_fma_f32 v184, -v180, v183, v182
	v_fmac_f32_e32 v183, v184, v181
	v_fma_f32 v180, -v180, v183, v182
	v_div_fmas_f32 v180, v180, v181, v183
	v_div_fixup_f32 v22, v180, v22, 1.0
	v_div_scale_f32 v180, s[100:101], v23, v23, 1.0
	v_rcp_f32_e32 v181, v180
	v_div_scale_f32 v182, vcc, 1.0, v23, 1.0
	v_fma_f32 v183, -v180, v181, 1.0
	v_fmac_f32_e32 v181, v183, v181
	v_mul_f32_e32 v183, v182, v181
	v_fma_f32 v184, -v180, v183, v182
	v_fmac_f32_e32 v183, v184, v181
	v_fma_f32 v180, -v180, v183, v182
	v_div_fmas_f32 v180, v180, v181, v183
	v_div_fixup_f32 v23, v180, v23, 1.0
	v_div_scale_f32 v180, s[100:101], v16, v16, 1.0
	v_rcp_f32_e32 v181, v180
	v_div_scale_f32 v182, vcc, 1.0, v16, 1.0
	v_fma_f32 v183, -v180, v181, 1.0
	v_fmac_f32_e32 v181, v183, v181
	v_mul_f32_e32 v183, v182, v181
	v_fma_f32 v184, -v180, v183, v182
	v_fmac_f32_e32 v183, v184, v181
	v_fma_f32 v180, -v180, v183, v182
	v_div_fmas_f32 v180, v180, v181, v183
	v_div_fixup_f32 v16, v180, v16, 1.0
	v_div_scale_f32 v180, s[100:101], v17, v17, 1.0
	v_rcp_f32_e32 v181, v180
	v_div_scale_f32 v182, vcc, 1.0, v17, 1.0
	v_fma_f32 v183, -v180, v181, 1.0
	v_fmac_f32_e32 v181, v183, v181
	v_mul_f32_e32 v183, v182, v181
	v_fma_f32 v184, -v180, v183, v182
	v_fmac_f32_e32 v183, v184, v181
	v_fma_f32 v180, -v180, v183, v182
	v_div_fmas_f32 v180, v180, v181, v183
	v_div_fixup_f32 v17, v180, v17, 1.0
	v_div_scale_f32 v180, s[100:101], v18, v18, 1.0
	v_rcp_f32_e32 v181, v180
	v_div_scale_f32 v182, vcc, 1.0, v18, 1.0
	v_fma_f32 v183, -v180, v181, 1.0
	v_fmac_f32_e32 v181, v183, v181
	v_mul_f32_e32 v183, v182, v181
	v_fma_f32 v184, -v180, v183, v182
	v_fmac_f32_e32 v183, v184, v181
	v_fma_f32 v180, -v180, v183, v182
	v_div_fmas_f32 v180, v180, v181, v183
	v_div_fixup_f32 v18, v180, v18, 1.0
	v_div_scale_f32 v180, s[100:101], v19, v19, 1.0
	v_rcp_f32_e32 v181, v180
	v_div_scale_f32 v182, vcc, 1.0, v19, 1.0
	v_fma_f32 v183, -v180, v181, 1.0
	v_fmac_f32_e32 v181, v183, v181
	v_mul_f32_e32 v183, v182, v181
	v_fma_f32 v184, -v180, v183, v182
	v_fmac_f32_e32 v183, v184, v181
	v_fma_f32 v180, -v180, v183, v182
	v_div_fmas_f32 v180, v180, v181, v183
	v_div_fixup_f32 v19, v180, v19, 1.0
	v_mul_f32_e32 v20, s0, v20
	v_mul_f32_e32 v21, s0, v21
	v_mul_f32_e32 v22, s0, v22
	v_mul_f32_e32 v23, s0, v23
	v_mul_f32_e32 v16, s0, v16
	v_mul_f32_e32 v17, s0, v17
	v_mul_f32_e32 v18, s0, v18
	v_mul_f32_e32 v19, s0, v19
	s_mov_b64 s[98:99], 0x24000
	v_lshl_add_u64 v[158:159], v[156:157], 0, s[98:99]
	v_cvt_pk_bf16_f32 v192, v20, v21
	v_cvt_pk_bf16_f32 v193, v22, v23
	v_cvt_pk_bf16_f32 v194, v16, v17
	v_cvt_pk_bf16_f32 v195, v18, v19
	global_store_dwordx4 v[158:159], v[192:195], off offset:256
	v_pk_add_f32 v[12:13], v[12:13], v[172:173]
	v_pk_add_f32 v[14:15], v[14:15], v[174:175]
	v_pk_add_f32 v[8:9], v[8:9], v[176:177]
	v_pk_add_f32 v[10:11], v[10:11], v[178:179]
	v_mul_f32_e32 v12, 0xbfb8aa3b, v12
	v_mul_f32_e32 v13, 0xbfb8aa3b, v13
	v_mul_f32_e32 v14, 0xbfb8aa3b, v14
	v_mul_f32_e32 v15, 0xbfb8aa3b, v15
	v_mul_f32_e32 v8, 0xbfb8aa3b, v8
	v_mul_f32_e32 v9, 0xbfb8aa3b, v9
	v_mul_f32_e32 v10, 0xbfb8aa3b, v10
	v_mul_f32_e32 v11, 0xbfb8aa3b, v11
	v_exp_f32_e32 v12, v12
	v_exp_f32_e32 v13, v13
	v_exp_f32_e32 v14, v14
	v_exp_f32_e32 v15, v15
	v_exp_f32_e32 v8, v8
	v_exp_f32_e32 v9, v9
	v_exp_f32_e32 v10, v10
	v_exp_f32_e32 v11, v11
	v_pk_add_f32 v[12:13], v[12:13], 1.0 op_sel_hi:[1,0]
	v_pk_add_f32 v[14:15], v[14:15], 1.0 op_sel_hi:[1,0]
	v_pk_add_f32 v[8:9], v[8:9], 1.0 op_sel_hi:[1,0]
	v_pk_add_f32 v[10:11], v[10:11], 1.0 op_sel_hi:[1,0]
	v_div_scale_f32 v180, s[100:101], v12, v12, 1.0
	v_rcp_f32_e32 v181, v180
	v_div_scale_f32 v182, vcc, 1.0, v12, 1.0
	v_fma_f32 v183, -v180, v181, 1.0
	v_fmac_f32_e32 v181, v183, v181
	v_mul_f32_e32 v183, v182, v181
	v_fma_f32 v184, -v180, v183, v182
	v_fmac_f32_e32 v183, v184, v181
	v_fma_f32 v180, -v180, v183, v182
	v_div_fmas_f32 v180, v180, v181, v183
	v_div_fixup_f32 v12, v180, v12, 1.0
	v_div_scale_f32 v180, s[100:101], v13, v13, 1.0
	v_rcp_f32_e32 v181, v180
	v_div_scale_f32 v182, vcc, 1.0, v13, 1.0
	v_fma_f32 v183, -v180, v181, 1.0
	v_fmac_f32_e32 v181, v183, v181
	v_mul_f32_e32 v183, v182, v181
	v_fma_f32 v184, -v180, v183, v182
	v_fmac_f32_e32 v183, v184, v181
	v_fma_f32 v180, -v180, v183, v182
	v_div_fmas_f32 v180, v180, v181, v183
	v_div_fixup_f32 v13, v180, v13, 1.0
	v_div_scale_f32 v180, s[100:101], v14, v14, 1.0
	v_rcp_f32_e32 v181, v180
	v_div_scale_f32 v182, vcc, 1.0, v14, 1.0
	v_fma_f32 v183, -v180, v181, 1.0
	v_fmac_f32_e32 v181, v183, v181
	v_mul_f32_e32 v183, v182, v181
	v_fma_f32 v184, -v180, v183, v182
	v_fmac_f32_e32 v183, v184, v181
	v_fma_f32 v180, -v180, v183, v182
	v_div_fmas_f32 v180, v180, v181, v183
	v_div_fixup_f32 v14, v180, v14, 1.0
	v_div_scale_f32 v180, s[100:101], v15, v15, 1.0
	v_rcp_f32_e32 v181, v180
	v_div_scale_f32 v182, vcc, 1.0, v15, 1.0
	v_fma_f32 v183, -v180, v181, 1.0
	v_fmac_f32_e32 v181, v183, v181
	v_mul_f32_e32 v183, v182, v181
	v_fma_f32 v184, -v180, v183, v182
	v_fmac_f32_e32 v183, v184, v181
	v_fma_f32 v180, -v180, v183, v182
	v_div_fmas_f32 v180, v180, v181, v183
	v_div_fixup_f32 v15, v180, v15, 1.0
	v_div_scale_f32 v180, s[100:101], v8, v8, 1.0
	v_rcp_f32_e32 v181, v180
	v_div_scale_f32 v182, vcc, 1.0, v8, 1.0
	v_fma_f32 v183, -v180, v181, 1.0
	v_fmac_f32_e32 v181, v183, v181
	v_mul_f32_e32 v183, v182, v181
	v_fma_f32 v184, -v180, v183, v182
	v_fmac_f32_e32 v183, v184, v181
	v_fma_f32 v180, -v180, v183, v182
	v_div_fmas_f32 v180, v180, v181, v183
	v_div_fixup_f32 v8, v180, v8, 1.0
; __device__ __forceinline__ float sigmoidf_(float x) { return 1.f / (1.f + __expf(-x)); }
; __device__ __forceinline__ unsigned cvt_pk_bf16(float lo, float hi) { const f32x2c v = {lo, hi}; const bf16x2c b = __builtin_convertvector(v, bf16x2c); return __builtin_bit_cast(unsigned, b); }
;     __device__ __forceinline__ void operator()(const f32x4 (&acc)[2][2][4][2], const Unit& u, int wr, int wc, int fr, int fq) const {
;     ...
;                 for (int m = 0; m < 4; ++m) { const size_t row = (size_t)(row0 + ai * HALF + m * 16);
;                     const f32x4 v0 = acc[ai][bj][m][0] + b0, v1 = acc[ai][bj][m][1] + b1; float o[8];
; #pragma unroll
;                     for (int e = 0; e < 8; ++e) { float x = (e < 4) ? v0[e & 3] : v1[e & 3];
;                         if (kind == 0) x = -0.6065306597126334f * sigmoidf_(x);
;                         else if (kind == 1) x = sigmoidf_(x);
;                         o[e] = x; }
;                     u32x4 w; w.x = cvt_pk_bf16(o[0], o[1]); w.y = cvt_pk_bf16(o[2], o[3]); w.z = cvt_pk_bf16(o[4], o[5]); w.w = cvt_pk_bf16(o[6], o[7]);
;                     *(u32x4*)(O + row * 512 + col) = w; } }
	v_div_scale_f32 v180, s[100:101], v9, v9, 1.0
	v_rcp_f32_e32 v181, v180
	v_div_scale_f32 v182, vcc, 1.0, v9, 1.0
	v_fma_f32 v183, -v180, v181, 1.0
	v_fmac_f32_e32 v181, v183, v181
	v_mul_f32_e32 v183, v182, v181
	v_fma_f32 v184, -v180, v183, v182
	v_fmac_f32_e32 v183, v184, v181
	v_fma_f32 v180, -v180, v183, v182
	v_div_fmas_f32 v180, v180, v181, v183
	v_div_fixup_f32 v9, v180, v9, 1.0
	v_div_scale_f32 v180, s[100:101], v10, v10, 1.0
	v_rcp_f32_e32 v181, v180
	v_div_scale_f32 v182, vcc, 1.0, v10, 1.0
	v_fma_f32 v183, -v180, v181, 1.0
	v_fmac_f32_e32 v181, v183, v181
	v_mul_f32_e32 v183, v182, v181
	v_fma_f32 v184, -v180, v183, v182
	v_fmac_f32_e32 v183, v184, v181
	v_fma_f32 v180, -v180, v183, v182
	v_div_fmas_f32 v180, v180, v181, v183
	v_div_fixup_f32 v10, v180, v10, 1.0
	v_div_scale_f32 v180, s[100:101], v11, v11, 1.0
	v_rcp_f32_e32 v181, v180
	v_div_scale_f32 v182, vcc, 1.0, v11, 1.0
	v_fma_f32 v183, -v180, v181, 1.0
	v_fmac_f32_e32 v181, v183, v181
	v_mul_f32_e32 v183, v182, v181
	v_fma_f32 v184, -v180, v183, v182
	v_fmac_f32_e32 v183, v184, v181
	v_fma_f32 v180, -v180, v183, v182
	v_div_fmas_f32 v180, v180, v181, v183
	v_div_fixup_f32 v11, v180, v11, 1.0
	v_mul_f32_e32 v12, s0, v12
	v_mul_f32_e32 v13, s0, v13
	v_mul_f32_e32 v14, s0, v14
	v_mul_f32_e32 v15, s0, v15
	v_mul_f32_e32 v8, s0, v8
	v_mul_f32_e32 v9, s0, v9
	v_mul_f32_e32 v10, s0, v10
	v_mul_f32_e32 v11, s0, v11
	s_mov_b64 s[98:99], 0x28000
	v_lshl_add_u64 v[158:159], v[156:157], 0, s[98:99]
	v_cvt_pk_bf16_f32 v188, v12, v13
	v_cvt_pk_bf16_f32 v189, v14, v15
	v_cvt_pk_bf16_f32 v190, v8, v9
	v_cvt_pk_bf16_f32 v191, v10, v11
	global_store_dwordx4 v[158:159], v[188:191], off offset:256
	v_pk_add_f32 v[4:5], v[4:5], v[172:173]
	v_pk_add_f32 v[6:7], v[6:7], v[174:175]
	v_pk_add_f32 v[0:1], v[0:1], v[176:177]
	v_pk_add_f32 v[2:3], v[2:3], v[178:179]
	v_mul_f32_e32 v4, 0xbfb8aa3b, v4
	v_mul_f32_e32 v5, 0xbfb8aa3b, v5
	v_mul_f32_e32 v6, 0xbfb8aa3b, v6
	v_mul_f32_e32 v7, 0xbfb8aa3b, v7
	v_mul_f32_e32 v0, 0xbfb8aa3b, v0
	v_mul_f32_e32 v1, 0xbfb8aa3b, v1
	v_mul_f32_e32 v2, 0xbfb8aa3b, v2
	v_mul_f32_e32 v3, 0xbfb8aa3b, v3
	v_exp_f32_e32 v4, v4
	v_exp_f32_e32 v5, v5
	v_exp_f32_e32 v6, v6
	v_exp_f32_e32 v7, v7
	v_exp_f32_e32 v0, v0
	v_exp_f32_e32 v1, v1
	v_exp_f32_e32 v2, v2
	v_exp_f32_e32 v3, v3
	v_pk_add_f32 v[4:5], v[4:5], 1.0 op_sel_hi:[1,0]
	v_pk_add_f32 v[6:7], v[6:7], 1.0 op_sel_hi:[1,0]
	v_pk_add_f32 v[0:1], v[0:1], 1.0 op_sel_hi:[1,0]
	v_pk_add_f32 v[2:3], v[2:3], 1.0 op_sel_hi:[1,0]
	v_div_scale_f32 v180, s[100:101], v4, v4, 1.0
	v_rcp_f32_e32 v181, v180
	v_div_scale_f32 v182, vcc, 1.0, v4, 1.0
	v_fma_f32 v183, -v180, v181, 1.0
	v_fmac_f32_e32 v181, v183, v181
	v_mul_f32_e32 v183, v182, v181
	v_fma_f32 v184, -v180, v183, v182
	v_fmac_f32_e32 v183, v184, v181
	v_fma_f32 v180, -v180, v183, v182
	v_div_fmas_f32 v180, v180, v181, v183
	v_div_fixup_f32 v4, v180, v4, 1.0
	v_div_scale_f32 v180, s[100:101], v5, v5, 1.0
	v_rcp_f32_e32 v181, v180
	v_div_scale_f32 v182, vcc, 1.0, v5, 1.0
	v_fma_f32 v183, -v180, v181, 1.0
	v_fmac_f32_e32 v181, v183, v181
	v_mul_f32_e32 v183, v182, v181
	v_fma_f32 v184, -v180, v183, v182
	v_fmac_f32_e32 v183, v184, v181
	v_fma_f32 v180, -v180, v183, v182
	v_div_fmas_f32 v180, v180, v181, v183
	v_div_fixup_f32 v5, v180, v5, 1.0
	v_div_scale_f32 v180, s[100:101], v6, v6, 1.0
	v_rcp_f32_e32 v181, v180
	v_div_scale_f32 v182, vcc, 1.0, v6, 1.0
	v_fma_f32 v183, -v180, v181, 1.0
	v_fmac_f32_e32 v181, v183, v181
	v_mul_f32_e32 v183, v182, v181
	v_fma_f32 v184, -v180, v183, v182
	v_fmac_f32_e32 v183, v184, v181
	v_fma_f32 v180, -v180, v183, v182
	v_div_fmas_f32 v180, v180, v181, v183
	v_div_fixup_f32 v6, v180, v6, 1.0
	v_div_scale_f32 v180, s[100:101], v7, v7, 1.0
	v_rcp_f32_e32 v181, v180
	v_div_scale_f32 v182, vcc, 1.0, v7, 1.0
	v_fma_f32 v183, -v180, v181, 1.0
	v_fmac_f32_e32 v181, v183, v181
	v_mul_f32_e32 v183, v182, v181
	v_fma_f32 v184, -v180, v183, v182
	v_fmac_f32_e32 v183, v184, v181
	v_fma_f32 v180, -v180, v183, v182
	v_div_fmas_f32 v180, v180, v181, v183
	v_div_fixup_f32 v7, v180, v7, 1.0
	v_div_scale_f32 v180, s[100:101], v0, v0, 1.0
	v_rcp_f32_e32 v181, v180
	v_div_scale_f32 v182, vcc, 1.0, v0, 1.0
	v_fma_f32 v183, -v180, v181, 1.0
	v_fmac_f32_e32 v181, v183, v181
	v_mul_f32_e32 v183, v182, v181
	v_fma_f32 v184, -v180, v183, v182
	v_fmac_f32_e32 v183, v184, v181
	v_fma_f32 v180, -v180, v183, v182
	v_div_fmas_f32 v180, v180, v181, v183
	v_div_fixup_f32 v0, v180, v0, 1.0
	v_div_scale_f32 v180, s[100:101], v1, v1, 1.0
	v_rcp_f32_e32 v181, v180
	v_div_scale_f32 v182, vcc, 1.0, v1, 1.0
	v_fma_f32 v183, -v180, v181, 1.0
	v_fmac_f32_e32 v181, v183, v181
	v_mul_f32_e32 v183, v182, v181
	v_fma_f32 v184, -v180, v183, v182
	v_fmac_f32_e32 v183, v184, v181
	v_fma_f32 v180, -v180, v183, v182
	v_div_fmas_f32 v180, v180, v181, v183
	v_div_fixup_f32 v1, v180, v1, 1.0
	v_div_scale_f32 v180, s[100:101], v2, v2, 1.0
	v_rcp_f32_e32 v181, v180
	v_div_scale_f32 v182, vcc, 1.0, v2, 1.0
	v_fma_f32 v183, -v180, v181, 1.0
	v_fmac_f32_e32 v181, v183, v181
	v_mul_f32_e32 v183, v182, v181
	v_fma_f32 v184, -v180, v183, v182
	v_fmac_f32_e32 v183, v184, v181
	v_fma_f32 v180, -v180, v183, v182
	v_div_fmas_f32 v180, v180, v181, v183
	v_div_fixup_f32 v2, v180, v2, 1.0
	v_div_scale_f32 v180, s[100:101], v3, v3, 1.0
	v_rcp_f32_e32 v181, v180
	v_div_scale_f32 v182, vcc, 1.0, v3, 1.0
	v_fma_f32 v183, -v180, v181, 1.0
	v_fmac_f32_e32 v181, v183, v181
	v_mul_f32_e32 v183, v182, v181
	v_fma_f32 v184, -v180, v183, v182
	v_fmac_f32_e32 v183, v184, v181
	v_fma_f32 v180, -v180, v183, v182
	v_div_fmas_f32 v180, v180, v181, v183
	v_div_fixup_f32 v3, v180, v3, 1.0
	v_mul_f32_e32 v4, s0, v4
	v_mul_f32_e32 v5, s0, v5
	v_mul_f32_e32 v6, s0, v6
	v_mul_f32_e32 v7, s0, v7
	v_mul_f32_e32 v0, s0, v0
	v_mul_f32_e32 v1, s0, v1
	v_mul_f32_e32 v2, s0, v2
	v_mul_f32_e32 v3, s0, v3
	s_mov_b64 s[98:99], 0x2c000
	v_lshl_add_u64 v[158:159], v[156:157], 0, s[98:99]
	v_cvt_pk_bf16_f32 v192, v4, v5
	v_cvt_pk_bf16_f32 v193, v6, v7
	v_cvt_pk_bf16_f32 v194, v0, v1
	v_cvt_pk_bf16_f32 v195, v2, v3
	global_store_dwordx4 v[158:159], v[192:195], off offset:256
	s_branch .Llora_done
; __device__ __forceinline__ float sigmoidf_(float x) { return 1.f / (1.f + __expf(-x)); }
; __device__ __forceinline__ unsigned cvt_pk_bf16(float lo, float hi) { const f32x2c v = {lo, hi}; const bf16x2c b = __builtin_convertvector(v, bf16x2c); return __builtin_bit_cast(unsigned, b); }
;     __device__ __forceinline__ void operator()(const f32x4 (&acc)[2][2][4][2], const Unit& u, int wr, int wc, int fr, int fq) const {
;     ...
;         for (int bj = 0; bj < 2; ++bj) { const int col = (col0 + bj * HALF) & 511;
;             f32x4 b0 = (f32x4){0.f, 0.f, 0.f, 0.f}, b1 = b0;
;             if (kind == 0) { b0 = *(const f32x4*)(w0 + col); b1 = *(const f32x4*)(w0 + col + 4); }
;             else if (kind == 1) { b0 = *(const f32x4*)(a0 + col); b1 = *(const f32x4*)(a0 + col + 4); }
; #pragma unroll
;             for (int ai = 0; ai < 2; ++ai)
; #pragma unroll
;                 for (int m = 0; m < 4; ++m) { const size_t row = (size_t)(row0 + ai * HALF + m * 16);
;                     const f32x4 v0 = acc[ai][bj][m][0] + b0, v1 = acc[ai][bj][m][1] + b1; float o[8];
; #pragma unroll
;                     for (int e = 0; e < 8; ++e) { float x = (e < 4) ? v0[e & 3] : v1[e & 3];
;                         if (kind == 0) x = -0.6065306597126334f * sigmoidf_(x);
;                         else if (kind == 1) x = sigmoidf_(x);
;                         o[e] = x; }
;                     u32x4 w; w.x = cvt_pk_bf16(o[0], o[1]); w.y = cvt_pk_bf16(o[2], o[3]); w.z = cvt_pk_bf16(o[4], o[5]); w.w = cvt_pk_bf16(o[6], o[7]);
;                     *(u32x4*)(O + row * 512 + col) = w; } }
.Llora_g:
	v_cvt_pk_bf16_f32 v188, v132, v133
	v_cvt_pk_bf16_f32 v189, v134, v135
	v_cvt_pk_bf16_f32 v190, v128, v129
	v_cvt_pk_bf16_f32 v191, v130, v131
	global_store_dwordx4 v[156:157], v[188:191], off
	s_mov_b64 s[98:99], 0x4000
	v_lshl_add_u64 v[158:159], v[156:157], 0, s[98:99]
	v_cvt_pk_bf16_f32 v192, v124, v125
	v_cvt_pk_bf16_f32 v193, v126, v127
	v_cvt_pk_bf16_f32 v194, v120, v121
	v_cvt_pk_bf16_f32 v195, v122, v123
	global_store_dwordx4 v[158:159], v[192:195], off
	s_mov_b64 s[98:99], 0x8000
	v_lshl_add_u64 v[158:159], v[156:157], 0, s[98:99]
	v_cvt_pk_bf16_f32 v188, v116, v117
	v_cvt_pk_bf16_f32 v189, v118, v119
	v_cvt_pk_bf16_f32 v190, v112, v113
	v_cvt_pk_bf16_f32 v191, v114, v115
	global_store_dwordx4 v[158:159], v[188:191], off
	s_mov_b64 s[98:99], 0xc000
	v_lshl_add_u64 v[158:159], v[156:157], 0, s[98:99]
	v_cvt_pk_bf16_f32 v192, v108, v109
	v_cvt_pk_bf16_f32 v193, v110, v111
	v_cvt_pk_bf16_f32 v194, v104, v105
	v_cvt_pk_bf16_f32 v195, v106, v107
	global_store_dwordx4 v[158:159], v[192:195], off
	s_mov_b64 s[98:99], 0x20000
	v_lshl_add_u64 v[158:159], v[156:157], 0, s[98:99]
	v_cvt_pk_bf16_f32 v188, v100, v101
	v_cvt_pk_bf16_f32 v189, v102, v103
	v_cvt_pk_bf16_f32 v190, v96, v97
	v_cvt_pk_bf16_f32 v191, v98, v99
	global_store_dwordx4 v[158:159], v[188:191], off
	s_mov_b64 s[98:99], 0x24000
	v_lshl_add_u64 v[158:159], v[156:157], 0, s[98:99]
	v_cvt_pk_bf16_f32 v192, v92, v93
	v_cvt_pk_bf16_f32 v193, v94, v95
	v_cvt_pk_bf16_f32 v194, v84, v85
	v_cvt_pk_bf16_f32 v195, v86, v87
	global_store_dwordx4 v[158:159], v[192:195], off
	s_mov_b64 s[98:99], 0x28000
	v_lshl_add_u64 v[158:159], v[156:157], 0, s[98:99]
	v_cvt_pk_bf16_f32 v188, v76, v77
	v_cvt_pk_bf16_f32 v189, v78, v79
	v_cvt_pk_bf16_f32 v190, v72, v73
	v_cvt_pk_bf16_f32 v191, v74, v75
	global_store_dwordx4 v[158:159], v[188:191], off
	s_mov_b64 s[98:99], 0x2c000
	v_lshl_add_u64 v[158:159], v[156:157], 0, s[98:99]
	v_cvt_pk_bf16_f32 v192, v68, v69
	v_cvt_pk_bf16_f32 v193, v70, v71
	v_cvt_pk_bf16_f32 v194, v64, v65
	v_cvt_pk_bf16_f32 v195, v66, v67
	global_store_dwordx4 v[158:159], v[192:195], off
	v_cvt_pk_bf16_f32 v188, v60, v61
	v_cvt_pk_bf16_f32 v189, v62, v63
	v_cvt_pk_bf16_f32 v190, v56, v57
	v_cvt_pk_bf16_f32 v191, v58, v59
	global_store_dwordx4 v[156:157], v[188:191], off offset:256
	s_mov_b64 s[98:99], 0x4000
	v_lshl_add_u64 v[158:159], v[156:157], 0, s[98:99]
	v_cvt_pk_bf16_f32 v192, v52, v53
	v_cvt_pk_bf16_f32 v193, v54, v55
	v_cvt_pk_bf16_f32 v194, v48, v49
	v_cvt_pk_bf16_f32 v195, v50, v51
	global_store_dwordx4 v[158:159], v[192:195], off offset:256
	s_mov_b64 s[98:99], 0x8000
	v_lshl_add_u64 v[158:159], v[156:157], 0, s[98:99]
	v_cvt_pk_bf16_f32 v188, v44, v45
	v_cvt_pk_bf16_f32 v189, v46, v47
	v_cvt_pk_bf16_f32 v190, v40, v41
	v_cvt_pk_bf16_f32 v191, v42, v43
	global_store_dwordx4 v[158:159], v[188:191], off offset:256
	s_mov_b64 s[98:99], 0xc000
	v_lshl_add_u64 v[158:159], v[156:157], 0, s[98:99]
	v_cvt_pk_bf16_f32 v192, v36, v37
	v_cvt_pk_bf16_f32 v193, v38, v39
	v_cvt_pk_bf16_f32 v194, v32, v33
	v_cvt_pk_bf16_f32 v195, v34, v35
	global_store_dwordx4 v[158:159], v[192:195], off offset:256
	s_mov_b64 s[98:99], 0x20000
	v_lshl_add_u64 v[158:159], v[156:157], 0, s[98:99]
	v_cvt_pk_bf16_f32 v188, v28, v29
	v_cvt_pk_bf16_f32 v189, v30, v31
	v_cvt_pk_bf16_f32 v190, v24, v25
	v_cvt_pk_bf16_f32 v191, v26, v27
	global_store_dwordx4 v[158:159], v[188:191], off offset:256
	s_mov_b64 s[98:99], 0x24000
	v_lshl_add_u64 v[158:159], v[156:157], 0, s[98:99]
	v_cvt_pk_bf16_f32 v192, v20, v21
	v_cvt_pk_bf16_f32 v193, v22, v23
	v_cvt_pk_bf16_f32 v194, v16, v17
	v_cvt_pk_bf16_f32 v195, v18, v19
	global_store_dwordx4 v[158:159], v[192:195], off offset:256
	s_mov_b64 s[98:99], 0x28000
	v_lshl_add_u64 v[158:159], v[156:157], 0, s[98:99]
	v_cvt_pk_bf16_f32 v188, v12, v13
	v_cvt_pk_bf16_f32 v189, v14, v15
	v_cvt_pk_bf16_f32 v190, v8, v9
	v_cvt_pk_bf16_f32 v191, v10, v11
	global_store_dwordx4 v[158:159], v[188:191], off offset:256
	s_mov_b64 s[98:99], 0x2c000
	v_lshl_add_u64 v[158:159], v[156:157], 0, s[98:99]
	v_cvt_pk_bf16_f32 v192, v4, v5
	v_cvt_pk_bf16_f32 v193, v6, v7
	v_cvt_pk_bf16_f32 v194, v0, v1
	v_cvt_pk_bf16_f32 v195, v2, v3
	global_store_dwordx4 v[158:159], v[192:195], off offset:256
.Llora_done:
	s_cmp_eq_u32 s9, 5
	s_mov_b64 s[0:1], -1
	s_cbranch_scc1 .LBB0_559
	s_andn2_b64 vcc, exec, s[18:19]
	s_cbranch_vccnz .LBB0_558
	s_barrier
	s_branch .LBB0_558
